# speedup vs baseline: 1.0691x; 1.0045x over previous
.LBB0_11:
	v_bfe_u32 v3, v0, 5, 1
	v_lshlrev_b32_e32 v4, 8, v0
	v_and_b32_e32 v4, 0x1f00, v4
	v_and_b32_e32 v5, 7, v0
	v_bitop3_b32 v6, v3, v0, 7 bitop3:0x78
	v_lshl_or_b32 v64, v6, 4, v4
	v_bitop3_b32 v6, v3, v5, 2 bitop3:0x36
	v_lshl_or_b32 v65, v6, 4, v4
	v_bitop3_b32 v6, v3, v5, 4 bitop3:0x36
	v_bitop3_b32 v5, v3, v5, 6 bitop3:0x36
	v_lshl_or_b32 v66, v6, 4, v4
	v_lshl_or_b32 v67, v5, 4, v4
	v_and_b32_e32 v4, 3, v0
	v_lshlrev_b32_e32 v6, 4, v0
	v_lshlrev_b32_e32 v5, 3, v4
	v_and_b32_e32 v6, 0xc0, v6
	v_lshlrev_b32_e32 v8, 1, v0
	v_lshlrev_b32_e32 v9, 8, v3
	v_bfe_u32 v7, v0, 4, 2
	v_and_b32_e32 v8, 32, v8
	v_or3_b32 v5, v5, v9, v6
	s_mov_b32 s0, 0x8000
	v_or3_b32 v184, v5, v8, s0
	v_lshlrev_b32_e32 v5, 8, v7
	v_xor_b32_e32 v6, v7, v1
	s_cmp_lg_u32 0, -1
	v_lshl_or_b32 v222, v6, 4, v5
	v_bitop3_b32 v1, v7, v1, 4 bitop3:0x36
	s_mov_b32 m0, s29
	s_nop 0
	buffer_load_dwordx4 v222, s[12:15], s61 offen lds
	s_cselect_b32 s17, 0, 0
	v_lshl_or_b32 v223, v1, 4, v5
	s_add_i32 s20, s29, 0x400
	s_add_i32 s0, s61, 0x400
	s_mov_b32 m0, s20
	s_nop 0
	buffer_load_dwordx4 v223, s[12:15], s0 offen lds
	v_lshlrev_b32_e32 v0, 6, v0
	s_add_i32 s21, s29, 0x800
	s_add_i32 s0, s61, 0x800
	s_mov_b32 m0, s21
	s_nop 0
	buffer_load_dwordx4 v222, s[12:15], s0 offen lds
	v_and_b32_e32 v0, 0x700, v0
	v_lshlrev_b32_e32 v1, 6, v3
	v_lshlrev_b32_e32 v3, 4, v4
	s_add_i32 s22, s29, 0xc00
	s_add_i32 s1, s61, 0xc00
	s_mov_b32 m0, s22
	s_nop 0
	buffer_load_dwordx4 v223, s[12:15], s1 offen lds
	v_or3_b32 v196, v0, v1, v3
	s_add_i32 s2, s29, 0x8000
	s_mov_b32 m0, s2
	s_nop 0
	buffer_load_dwordx4 v196, s[4:7], s61 offen lds
	s_add_i32 s1, s2, 0x400
	s_add_i32 s3, s61, 0x80
	s_mov_b32 m0, s1
	s_nop 0
	buffer_load_dwordx4 v196, s[4:7], s3 offen lds
	s_add_i32 s1, s2, 0x800
	s_mov_b32 m0, s1
	s_nop 0
	buffer_load_dwordx4 v196, s[4:7], s0 offen lds
	s_add_i32 s0, s2, 0xc00
	s_add_i32 s1, s61, 0x880
	s_mov_b32 m0, s0
	s_nop 0
	buffer_load_dwordx4 v196, s[4:7], s1 offen lds
	s_add_i32 s3, s29, 0x4000
	s_add_i32 s19, s61, 0x4000
	s_mov_b32 m0, s3
	s_nop 0
	buffer_load_dwordx4 v222, s[12:15], s19 offen lds
	v_or_b32_e32 v2, 0x10000, v40
	v_add_u32_e32 v218, s17, v64
	v_add_u32_e32 v219, s17, v65
	v_add_u32_e32 v220, s17, v66
	v_add_u32_e32 v221, s17, v67
	s_add_i32 s10, s29, 0x4400
	s_add_i32 s0, s61, 0x4400
	s_mov_b32 m0, s10
	s_nop 0
	buffer_load_dwordx4 v223, s[12:15], s0 offen lds
	s_add_i32 s11, s29, 0x4800
	s_add_i32 s18, s61, 0x4800
	s_mov_b32 m0, s11
	s_nop 0
	buffer_load_dwordx4 v222, s[12:15], s18 offen lds
	v_add_u32_e32 v32, v2, v218
	v_add_u32_e32 v33, v2, v219
	v_add_u32_e32 v34, v2, v220
	v_add_u32_e32 v35, v2, v221
	s_add_i32 s16, s29, 0x4c00
	s_add_i32 s0, s61, 0x4c00
	s_mov_b32 m0, s16
	s_nop 0
	buffer_load_dwordx4 v223, s[12:15], s0 offen lds
	v_add_u32_e32 v212, s17, v184
	ds_read_b128 v[0:3], v32 offset:0
	ds_read_b128 v[4:7], v33 offset:0
	ds_read_b128 v[8:11], v34 offset:0
	ds_read_b128 v[12:15], v35 offset:0
	ds_read_b128 v[16:19], v32 offset:128
	ds_read_b128 v[20:23], v33 offset:128
	ds_read_b128 v[24:27], v34 offset:128
	ds_read_b128 v[28:31], v35 offset:128
	s_waitcnt lgkmcnt(0)
	v_accvgpr_write_b32 a[128], v0
	v_accvgpr_write_b32 a[129], v1
	v_accvgpr_write_b32 a[130], v2
	v_accvgpr_write_b32 a[131], v3
	v_accvgpr_write_b32 a[132], v4
	v_accvgpr_write_b32 a[133], v5
	v_accvgpr_write_b32 a[134], v6
	v_accvgpr_write_b32 a[135], v7
	v_accvgpr_write_b32 a[136], v8
	v_accvgpr_write_b32 a[137], v9
	v_accvgpr_write_b32 a[138], v10
	v_accvgpr_write_b32 a[139], v11
	v_accvgpr_write_b32 a[140], v12
	v_accvgpr_write_b32 a[141], v13
	v_accvgpr_write_b32 a[142], v14
	v_accvgpr_write_b32 a[143], v15
	v_accvgpr_write_b32 a[144], v16
	v_accvgpr_write_b32 a[145], v17
	v_accvgpr_write_b32 a[146], v18
	v_accvgpr_write_b32 a[147], v19
	v_accvgpr_write_b32 a[148], v20
	v_accvgpr_write_b32 a[149], v21
	v_accvgpr_write_b32 a[150], v22
	v_accvgpr_write_b32 a[151], v23
	v_accvgpr_write_b32 a[152], v24
	v_accvgpr_write_b32 a[153], v25
	v_accvgpr_write_b32 a[154], v26
	v_accvgpr_write_b32 a[155], v27
	v_accvgpr_write_b32 a[156], v28
	v_accvgpr_write_b32 a[157], v29
	v_accvgpr_write_b32 a[158], v30
	v_accvgpr_write_b32 a[159], v31
	ds_read_b128 v[0:3], v32 offset:8192
	ds_read_b128 v[4:7], v33 offset:8192
	ds_read_b128 v[8:11], v34 offset:8192
	ds_read_b128 v[12:15], v35 offset:8192
	ds_read_b128 v[16:19], v32 offset:8320
	ds_read_b128 v[20:23], v33 offset:8320
	ds_read_b128 v[24:27], v34 offset:8320
	ds_read_b128 v[28:31], v35 offset:8320
	s_waitcnt lgkmcnt(0)
	v_accvgpr_write_b32 a[160], v0
	v_accvgpr_write_b32 a[161], v1
	v_accvgpr_write_b32 a[162], v2
	v_accvgpr_write_b32 a[163], v3
	v_accvgpr_write_b32 a[164], v4
	v_accvgpr_write_b32 a[165], v5
	v_accvgpr_write_b32 a[166], v6
	v_accvgpr_write_b32 a[167], v7
	v_accvgpr_write_b32 a[168], v8
	v_accvgpr_write_b32 a[169], v9
	v_accvgpr_write_b32 a[170], v10
	v_accvgpr_write_b32 a[171], v11
	v_accvgpr_write_b32 a[172], v12
	v_accvgpr_write_b32 a[173], v13
	v_accvgpr_write_b32 a[174], v14
	v_accvgpr_write_b32 a[175], v15
	v_accvgpr_write_b32 a[176], v16
	v_accvgpr_write_b32 a[177], v17
	v_accvgpr_write_b32 a[178], v18
	v_accvgpr_write_b32 a[179], v19
	v_accvgpr_write_b32 a[180], v20
	v_accvgpr_write_b32 a[181], v21
	v_accvgpr_write_b32 a[182], v22
	v_accvgpr_write_b32 a[183], v23
	v_accvgpr_write_b32 a[184], v24
	v_accvgpr_write_b32 a[185], v25
	v_accvgpr_write_b32 a[186], v26
	v_accvgpr_write_b32 a[187], v27
	v_accvgpr_write_b32 a[188], v28
	v_accvgpr_write_b32 a[189], v29
	v_accvgpr_write_b32 a[190], v30
	v_accvgpr_write_b32 a[191], v31
	s_waitcnt vmcnt(0) lgkmcnt(0)
	s_barrier
	s_nop 0
	ds_read_b128 a[192:195], v218 offset:0
	s_nop 0
	ds_read_b128 a[196:199], v219 offset:0
	ds_read_b128 a[200:203], v220 offset:0
	ds_read_b128 a[204:207], v221 offset:0
	ds_read_b128 a[208:211], v218 offset:128
	ds_read_b128 a[212:215], v219 offset:128
	ds_read_b128 a[216:219], v220 offset:128
	ds_read_b128 a[220:223], v221 offset:128
	ds_read_b128 a[224:227], v218 offset:8192
	ds_read_b128 a[228:231], v219 offset:8192
	ds_read_b128 a[232:235], v220 offset:8192
	ds_read_b128 a[236:239], v221 offset:8192
	ds_read_b128 a[240:243], v218 offset:8320
	ds_read_b128 a[244:247], v219 offset:8320
	ds_read_b128 a[248:251], v220 offset:8320
	ds_read_b128 a[252:255], v221 offset:8320
	s_waitcnt lgkmcnt(0)
	v_mfma_f32_32x32x16_bf16 v[48:63], a[192:195], a[128:131], 0
	v_mfma_f32_32x32x16_bf16 v[32:47], a[192:195], a[160:163], 0
	v_mfma_f32_32x32x16_bf16 v[0:15], a[224:227], a[128:131], 0
	v_mfma_f32_32x32x16_bf16 v[16:31], a[224:227], a[160:163], 0
	v_mfma_f32_32x32x16_bf16 v[48:63], a[196:199], a[132:135], v[48:63]
	v_mfma_f32_32x32x16_bf16 v[32:47], a[196:199], a[164:167], v[32:47]
	v_mfma_f32_32x32x16_bf16 v[0:15], a[228:231], a[132:135], v[0:15]
	v_mfma_f32_32x32x16_bf16 v[16:31], a[228:231], a[164:167], v[16:31]
	v_mfma_f32_32x32x16_bf16 v[48:63], a[200:203], a[136:139], v[48:63]
	v_mfma_f32_32x32x16_bf16 v[32:47], a[200:203], a[168:171], v[32:47]
	v_mfma_f32_32x32x16_bf16 v[0:15], a[232:235], a[136:139], v[0:15]
	v_mfma_f32_32x32x16_bf16 v[16:31], a[232:235], a[168:171], v[16:31]
	v_mfma_f32_32x32x16_bf16 v[48:63], a[204:207], a[140:143], v[48:63]
	v_mfma_f32_32x32x16_bf16 v[32:47], a[204:207], a[172:175], v[32:47]
	v_mfma_f32_32x32x16_bf16 v[0:15], a[236:239], a[140:143], v[0:15]
	v_mfma_f32_32x32x16_bf16 v[16:31], a[236:239], a[172:175], v[16:31]
	v_mfma_f32_32x32x16_bf16 v[48:63], a[208:211], a[144:147], v[48:63]
	s_mov_b32 s27, s29
	v_mfma_f32_32x32x16_bf16 v[32:47], a[208:211], a[176:179], v[32:47]
	s_add_i32 s0, s62, 0x0
	s_mov_b32 s30, s0
	v_mfma_f32_32x32x16_bf16 v[0:15], a[240:243], a[144:147], v[0:15]
	s_mov_b32 s31, s20
	v_mfma_f32_32x32x16_bf16 v[16:31], a[240:243], a[176:179], v[16:31]
	s_add_i32 s33, s62, 0x400
	v_mfma_f32_32x32x16_bf16 v[48:63], a[212:215], a[148:151], v[48:63]
	s_mov_b32 s34, s21
	v_mfma_f32_32x32x16_bf16 v[32:47], a[212:215], a[180:183], v[32:47]
	s_add_i32 s1, s62, 0x800
	s_mov_b32 s35, s1
	v_mfma_f32_32x32x16_bf16 v[0:15], a[244:247], a[148:151], v[0:15]
	s_mov_b32 s36, s22
	v_mfma_f32_32x32x16_bf16 v[16:31], a[244:247], a[180:183], v[16:31]
	s_add_i32 s37, s62, 0xc00
	v_mfma_f32_32x32x16_bf16 v[48:63], a[216:219], a[152:155], v[48:63]
	s_add_i32 s23, s29, 0xc000
	s_mov_b32 s38, s23
	v_mfma_f32_32x32x16_bf16 v[32:47], a[216:219], a[184:187], v[32:47]
	v_mfma_f32_32x32x16_bf16 v[0:15], a[248:251], a[152:155], v[0:15]
	s_add_i32 s24, s29, 0xc400
	s_mov_b32 s39, s24
	v_mfma_f32_32x32x16_bf16 v[16:31], a[248:251], a[184:187], v[16:31]
	s_add_i32 s40, s61, 0x4080
	v_mfma_f32_32x32x16_bf16 v[48:63], a[220:223], a[156:159], v[48:63]
	s_add_i32 s25, s29, 0xc800
	s_mov_b32 s41, s25
	v_mfma_f32_32x32x16_bf16 v[32:47], a[220:223], a[188:191], v[32:47]
	v_mfma_f32_32x32x16_bf16 v[0:15], a[252:255], a[156:159], v[0:15]
	s_add_i32 s26, s29, 0xcc00
	s_mov_b32 s42, s26
	v_mfma_f32_32x32x16_bf16 v[16:31], a[252:255], a[188:191], v[16:31]
	s_add_i32 s43, s61, 0x4880
	s_waitcnt vmcnt(0) lgkmcnt(0)
	s_barrier
	s_nop 0
	s_mov_b32 m0, s27
	s_nop 0
	buffer_load_dwordx4 v222, s[12:15], s30 offen lds
	s_mov_b32 m0, s31
	s_nop 0
	buffer_load_dwordx4 v223, s[12:15], s33 offen lds
	s_addk_i32 s17, 0x4000
	v_add_u32_e32 v217, s17, v64
	ds_read_b128 a[192:195], v217 offset:0
	s_mov_b32 m0, s34
	s_nop 0
	buffer_load_dwordx4 v222, s[12:15], s35 offen lds
	v_add_u32_e32 v199, s17, v65
	ds_read_b128 a[196:199], v199 offset:0
	s_mov_b32 m0, s36
	s_nop 0
	buffer_load_dwordx4 v223, s[12:15], s37 offen lds
	v_add_u32_e32 v198, s17, v66
	ds_read_b128 a[200:203], v198 offset:0
	s_mov_b32 m0, s38
	s_nop 0
	buffer_load_dwordx4 v196, s[4:7], s19 offen lds
	v_add_u32_e32 v197, s17, v67
	ds_read_b128 a[204:207], v197 offset:0
	s_mov_b32 m0, s39
	s_nop 0
	buffer_load_dwordx4 v196, s[4:7], s40 offen lds
	ds_read_b128 a[208:211], v217 offset:128
	s_mov_b32 m0, s41
	s_nop 0
	buffer_load_dwordx4 v196, s[4:7], s18 offen lds
	ds_read_b128 a[212:215], v199 offset:128
	s_mov_b32 m0, s42
	s_nop 0
	buffer_load_dwordx4 v196, s[4:7], s43 offen lds
	ds_read_b128 a[216:219], v198 offset:128
	ds_read_b128 a[220:223], v197 offset:128
	v_cvt_pk_bf16_f32 v248, v248, v249
	v_cvt_pk_bf16_f32 v249, v250, v251
	v_cvt_pk_bf16_f32 v250, v252, v253
	v_cvt_pk_bf16_f32 v251, v254, v255
	v_lshrrev_b32_e32 v252, 1, v208
	buffer_store_dwordx4 v[248:251], v252, s[12:15], s56 offen sc1
	s_nop 1
	global_load_dwordx4 v[248:251], v208, s[74:75] nt
	global_load_dwordx4 v[252:255], v208, s[74:75] offset:16 nt
	s_add_u32 s74, s74, 0x2000
	s_addc_u32 s75, s75, 0
	v_max3_f32 v64, v48, v49, v0
	v_max3_f32 v65, v50, v51, v1
	v_max3_f32 v64, v64, v2, v3
	ds_read_b128 a[224:227], v217 offset:8192
	v_max3_f32 v64, v64, v52, v53
	v_max3_f32 v65, v65, v54, v55
	v_max3_f32 v64, v64, v4, v5
	v_max3_f32 v65, v65, v6, v7
	ds_read_b128 a[228:231], v199 offset:8192
	v_max3_f32 v64, v64, v56, v57
	v_max3_f32 v65, v65, v58, v59
	v_max3_f32 v64, v64, v8, v9
	v_max3_f32 v65, v65, v10, v11
	ds_read_b128 a[232:235], v198 offset:8192
	v_max3_f32 v64, v64, v60, v61
	v_max3_f32 v65, v65, v62, v63
	v_max3_f32 v64, v64, v12, v13
	v_max3_f32 v65, v65, v14, v15
	ds_read_b128 a[236:239], v197 offset:8192
	v_max3_f32 v66, v32, v33, v16
	v_max3_f32 v67, v34, v35, v17
	v_max3_f32 v66, v66, v18, v19
	ds_read_b128 a[240:243], v217 offset:8320
	v_max3_f32 v66, v66, v36, v37
	v_max3_f32 v67, v67, v38, v39
	v_max3_f32 v66, v66, v20, v21
	v_max3_f32 v67, v67, v22, v23
	ds_read_b128 a[244:247], v199 offset:8320
	v_max3_f32 v66, v66, v40, v41
	v_max3_f32 v67, v67, v42, v43
	v_max3_f32 v66, v66, v24, v25
	v_max3_f32 v67, v67, v26, v27
	ds_read_b128 a[248:251], v198 offset:8320
	v_max3_f32 v66, v66, v44, v45
	v_max3_f32 v67, v67, v46, v47
	v_max3_f32 v66, v66, v28, v29
	v_max3_f32 v67, v67, v30, v31
	ds_read_b128 a[252:255], v197 offset:8320
	v_max_f32_e32 v64, v64, v65
	v_mov_b32_e32 v65, v64
	s_nop 1
	v_permlane32_swap_b32_e32 v64, v65
	v_max_f32_e32 v214, v64, v65
	v_max_f32_e32 v64, v66, v67
	v_mov_b32_e32 v65, v64
	s_nop 1
	v_permlane32_swap_b32_e32 v64, v65
	v_max_f32_e32 v213, v64, v65
	v_sub_f32_e32 v64, v0, v214
	v_mbcnt_lo_u32_b32 v0, -1, 0
	v_mbcnt_hi_u32_b32 v0, -1, v0
	v_sub_f32_e32 v65, v1, v214
	v_xor_b32_e32 v1, 0x80000000, v214
	v_cmp_gt_u32_e32 vcc, 32, v0
	v_sub_f32_e32 v128, v2, v214
	v_sub_f32_e32 v129, v3, v214
	v_sub_f32_e32 v130, v4, v214
	v_sub_f32_e32 v131, v5, v214
	v_sub_f32_e32 v132, v6, v214
	v_sub_f32_e32 v133, v7, v214
	v_sub_f32_e32 v134, v8, v214
	v_sub_f32_e32 v135, v9, v214
	v_sub_f32_e32 v136, v10, v214
	v_sub_f32_e32 v137, v11, v214
	v_sub_f32_e32 v138, v12, v214
	v_sub_f32_e32 v139, v13, v214
	v_sub_f32_e32 v140, v14, v214
	v_sub_f32_e32 v141, v15, v214
	v_sub_f32_e32 v142, v16, v213
	v_mov_b32_e32 v211, 1.0
	v_sub_f32_e32 v143, v17, v213
	v_xor_b32_e32 v17, 0x80000000, v213
	v_cndmask_b32_e64 v0, 0, 1.0, vcc
	s_nop 1
	v_mfma_f32_32x32x2_f32 v[0:15], v0, v1, 0
	v_mbcnt_lo_u32_b32 v16, -1, 0
	v_mbcnt_hi_u32_b32 v16, -1, v16
	v_sub_f32_e32 v48, v48, v214
	v_sub_f32_e32 v49, v49, v214
	v_sub_f32_e32 v50, v50, v214
	v_sub_f32_e32 v51, v51, v214
	v_sub_f32_e32 v52, v52, v214
	v_sub_f32_e32 v53, v53, v214
	v_sub_f32_e32 v54, v54, v214
	v_sub_f32_e32 v55, v55, v214
	v_sub_f32_e32 v56, v56, v214
	v_sub_f32_e32 v57, v57, v214
	v_sub_f32_e32 v58, v58, v214
	v_sub_f32_e32 v59, v59, v214
	v_sub_f32_e32 v60, v60, v214
	v_sub_f32_e32 v61, v61, v214
	v_sub_f32_e32 v62, v62, v214
	v_sub_f32_e32 v63, v63, v214
	v_sub_f32_e32 v32, v32, v213
	v_sub_f32_e32 v33, v33, v213
	v_sub_f32_e32 v34, v34, v213
	v_cmp_gt_u32_e32 vcc, 32, v16
	v_sub_f32_e32 v35, v35, v213
	v_sub_f32_e32 v36, v36, v213
	v_sub_f32_e32 v37, v37, v213
	v_sub_f32_e32 v38, v38, v213
	v_sub_f32_e32 v39, v39, v213
	v_sub_f32_e32 v40, v40, v213
	v_sub_f32_e32 v41, v41, v213
	v_sub_f32_e32 v42, v42, v213
	v_sub_f32_e32 v43, v43, v213
	v_sub_f32_e32 v44, v44, v213
	v_sub_f32_e32 v45, v45, v213
	v_sub_f32_e32 v46, v46, v213
	v_sub_f32_e32 v47, v47, v213
	v_sub_f32_e32 v144, v18, v213
	v_sub_f32_e32 v145, v19, v213
	v_sub_f32_e32 v146, v20, v213
	v_sub_f32_e32 v147, v21, v213
	v_sub_f32_e32 v183, v22, v213
	v_sub_f32_e32 v194, v23, v213
	v_cndmask_b32_e64 v16, 0, 1.0, vcc
	v_sub_f32_e32 v195, v24, v213
	v_sub_f32_e32 v215, v25, v213
	v_sub_f32_e32 v216, v26, v213
	v_sub_f32_e32 v224, v27, v213
	v_sub_f32_e32 v225, v28, v213
	v_sub_f32_e32 v226, v29, v213
	v_sub_f32_e32 v229, v30, v213
	v_sub_f32_e32 v230, v31, v213
	v_mfma_f32_32x32x2_f32 v[16:31], v16, v17, 0
	v_exp_f32_e32 v112, v48
	v_exp_f32_e32 v113, v49
	v_exp_f32_e32 v114, v50
	v_exp_f32_e32 v115, v51
	v_mov_b32_e32 v193, 0
	v_add_f32_e32 v48, v193, v112
	v_add_f32_e32 v49, v193, v113
	v_exp_f32_e32 v116, v52
	v_exp_f32_e32 v117, v53
	v_exp_f32_e32 v118, v54
	v_add_f32_e32 v48, v48, v114
	v_add_f32_e32 v49, v49, v115
	v_exp_f32_e32 v119, v55
	v_exp_f32_e32 v120, v56
	v_add_f32_e32 v48, v48, v116
	v_add_f32_e32 v49, v49, v117
	v_add_f32_e32 v48, v48, v118
	v_exp_f32_e32 v121, v57
	v_exp_f32_e32 v122, v58
	v_exp_f32_e32 v123, v59
	v_add_f32_e32 v49, v49, v119
	v_add_f32_e32 v48, v48, v120
	v_exp_f32_e32 v124, v60
	v_exp_f32_e32 v125, v61
	v_add_f32_e32 v49, v49, v121
	v_add_f32_e32 v48, v48, v122
	v_add_f32_e32 v49, v49, v123
	v_exp_f32_e32 v126, v62
	v_exp_f32_e32 v127, v63
	v_exp_f32_e32 v96, v32
	v_add_f32_e32 v32, v48, v124
	v_add_f32_e32 v48, v49, v125
	v_exp_f32_e32 v97, v33
	v_exp_f32_e32 v98, v34
	v_add_f32_e32 v231, v32, v126
	v_add_f32_e32 v232, v48, v127
	v_add_f32_e32 v32, v193, v96
	v_exp_f32_e32 v99, v35
	v_exp_f32_e32 v100, v36
	v_exp_f32_e32 v101, v37
	v_add_f32_e32 v33, v193, v97
	v_add_f32_e32 v32, v32, v98
	v_exp_f32_e32 v102, v38
	v_exp_f32_e32 v103, v39
	v_add_f32_e32 v33, v33, v99
	v_add_f32_e32 v32, v32, v100
	v_add_f32_e32 v33, v33, v101
	v_exp_f32_e32 v104, v40
	v_exp_f32_e32 v105, v41
	v_exp_f32_e32 v106, v42
	v_add_f32_e32 v32, v32, v102
	v_add_f32_e32 v33, v33, v103
	v_exp_f32_e32 v107, v43
	v_exp_f32_e32 v108, v44
	v_add_f32_e32 v32, v32, v104
	v_add_f32_e32 v33, v33, v105
	v_add_f32_e32 v32, v32, v106
	v_exp_f32_e32 v109, v45
	v_exp_f32_e32 v110, v46
	v_exp_f32_e32 v111, v47
	v_add_f32_e32 v33, v33, v107
	v_add_f32_e32 v32, v32, v108
	s_waitcnt lgkmcnt(0)
	v_add_f32_e32 v33, v33, v109
	v_add_f32_e32 v233, v32, v110
	v_add_f32_e32 v234, v33, v111
	v_mfma_f32_32x32x16_bf16 v[80:95], a[192:195], a[128:131], v[0:15]
	ds_read_b64_tr_b16 v[160:161], v212 offset:0
	v_exp_f32_e32 v235, v64
	v_exp_f32_e32 v236, v65
	v_cvt_pk_bf16_f32 v152, v112, v113
	v_mfma_f32_32x32x16_bf16 v[64:79], a[192:195], a[160:163], v[16:31]
	ds_read_b64_tr_b16 v[162:163], v212 offset:0x800
	v_exp_f32_e32 v237, v128
	v_exp_f32_e32 v238, v129
	v_cvt_pk_bf16_f32 v153, v114, v115
	v_exp_f32_e32 v115, v130
	v_mfma_f32_32x32x16_bf16 v[48:63], a[224:227], a[128:131], v[0:15]
	ds_read_b64_tr_b16 v[172:173], v212 offset:0x200
	v_exp_f32_e32 v239, v131
	v_cvt_pk_bf16_f32 v154, v116, v117
	v_mfma_f32_32x32x16_bf16 v[32:47], a[224:227], a[160:163], v[16:31]
	ds_read_b64_tr_b16 v[174:175], v212 offset:0xa00
	ds_read_b64_tr_b16 v[168:169], v212 offset:0x400
	v_exp_f32_e32 v240, v132
	v_exp_f32_e32 v241, v133
	v_cvt_pk_bf16_f32 v155, v118, v119
	v_exp_f32_e32 v185, v134
	v_exp_f32_e32 v186, v135
	v_mfma_f32_32x32x16_bf16 v[80:95], a[196:199], a[132:135], v[80:95]
	ds_read_b64_tr_b16 v[170:171], v212 offset:0xc00
	v_cvt_pk_bf16_f32 v128, v120, v121
	v_exp_f32_e32 v187, v136
	v_exp_f32_e32 v188, v137
	v_mfma_f32_32x32x16_bf16 v[64:79], a[196:199], a[164:167], v[64:79]
	ds_read_b64_tr_b16 v[176:177], v212 offset:0x600
	v_cvt_pk_bf16_f32 v129, v122, v123
	v_exp_f32_e32 v189, v138
	v_exp_f32_e32 v190, v139
	v_mfma_f32_32x32x16_bf16 v[48:63], a[228:231], a[132:135], v[48:63]
	ds_read_b64_tr_b16 v[178:179], v212 offset:0xe00
	v_cvt_pk_bf16_f32 v130, v124, v125
	v_mfma_f32_32x32x16_bf16 v[32:47], a[228:231], a[164:167], v[32:47]
	ds_read_b64_tr_b16 v[164:165], v212 offset:0x1000
	v_exp_f32_e32 v191, v140
	v_exp_f32_e32 v192, v141
	ds_read_b64_tr_b16 v[166:167], v212 offset:0x1800
	v_cvt_pk_bf16_f32 v131, v126, v127
	v_exp_f32_e32 v141, v142
	v_exp_f32_e32 v142, v143
	v_mfma_f32_32x32x16_bf16 v[80:95], a[200:203], a[136:139], v[80:95]
	ds_read_b64_tr_b16 v[156:157], v212 offset:0x1200
	v_cvt_pk_bf16_f32 v180, v96, v97
	v_exp_f32_e32 v143, v144
	v_mfma_f32_32x32x16_bf16 v[64:79], a[200:203], a[168:171], v[64:79]
	ds_read_b64_tr_b16 v[158:159], v212 offset:0x1a00
	v_exp_f32_e32 v242, v145
	v_cvt_pk_bf16_f32 v181, v98, v99
	v_mfma_f32_32x32x16_bf16 v[48:63], a[232:235], a[136:139], v[48:63]
	ds_read_b64_tr_b16 v[148:149], v212 offset:0x1400
	v_exp_f32_e32 v243, v146
	v_exp_f32_e32 v244, v147
	v_cvt_pk_bf16_f32 v182, v100, v101
	v_mfma_f32_32x32x16_bf16 v[32:47], a[232:235], a[168:171], v[32:47]
	ds_read_b64_tr_b16 v[150:151], v212 offset:0x1c00
	ds_read_b64_tr_b16 v[136:137], v212 offset:0x1600
	v_exp_f32_e32 v245, v183
	v_exp_f32_e32 v246, v194
	v_cvt_pk_bf16_f32 v183, v102, v103
	v_exp_f32_e32 v194, v195
	v_exp_f32_e32 v195, v215
	v_mfma_f32_32x32x16_bf16 v[80:95], a[204:207], a[140:143], v[80:95]
	ds_read_b64_tr_b16 v[138:139], v212 offset:0x1e00
	v_cvt_pk_bf16_f32 v144, v104, v105
	v_exp_f32_e32 v215, v216
	v_exp_f32_e32 v224, v224
	v_mfma_f32_32x32x16_bf16 v[64:79], a[204:207], a[172:175], v[64:79]
	ds_read_b64_tr_b16 v[132:133], v212 offset:0x2000
	v_cvt_pk_bf16_f32 v145, v106, v107
	v_exp_f32_e32 v227, v225
	v_exp_f32_e32 v228, v226
	v_mfma_f32_32x32x16_bf16 v[48:63], a[236:239], a[140:143], v[48:63]
	ds_read_b64_tr_b16 v[134:135], v212 offset:0x2800
	v_cvt_pk_bf16_f32 v146, v108, v109
	v_mfma_f32_32x32x16_bf16 v[32:47], a[236:239], a[172:175], v[32:47]
	ds_read_b64_tr_b16 v[124:125], v212 offset:0x2200
	v_exp_f32_e32 v229, v229
	v_exp_f32_e32 v230, v230
	ds_read_b64_tr_b16 v[126:127], v212 offset:0x2a00
	v_cvt_pk_bf16_f32 v147, v110, v111
	s_mov_b32 s27, s3
	v_mfma_f32_32x32x16_bf16 v[80:95], a[208:211], a[144:147], v[80:95]
	ds_read_b64_tr_b16 v[120:121], v212 offset:0x2400
	v_cvt_pk_bf16_f32 v112, v235, v236
	v_add_f32_e32 v96, v231, v235
	v_add_f32_e32 v97, v232, v236
	s_add_i32 s30, s62, 0x4000
	v_mfma_f32_32x32x16_bf16 v[64:79], a[208:211], a[176:179], v[64:79]
	ds_read_b64_tr_b16 v[122:123], v212 offset:0x2c00
	v_cvt_pk_bf16_f32 v113, v237, v238
	v_add_f32_e32 v96, v96, v237
	v_add_f32_e32 v97, v97, v238
	s_mov_b32 s31, s10
	v_mfma_f32_32x32x16_bf16 v[48:63], a[240:243], a[144:147], v[48:63]
	ds_read_b64_tr_b16 v[116:117], v212 offset:0x2600
	v_cvt_pk_bf16_f32 v114, v115, v239
	v_add_f32_e32 v96, v96, v115
	v_add_f32_e32 v97, v97, v239
	s_add_i32 s33, s62, 0x4400
	v_mfma_f32_32x32x16_bf16 v[32:47], a[240:243], a[176:179], v[32:47]
	ds_read_b64_tr_b16 v[118:119], v212 offset:0x2e00
	ds_read_b64_tr_b16 v[104:105], v212 offset:0x3000
	v_cvt_pk_bf16_f32 v115, v240, v241
	v_add_f32_e32 v96, v96, v240
	v_add_f32_e32 v97, v97, v241
	s_mov_b32 s34, s11
	v_mfma_f32_32x32x16_bf16 v[80:95], a[212:215], a[148:151], v[80:95]
	ds_read_b64_tr_b16 v[106:107], v212 offset:0x3800
	v_add_f32_e32 v96, v96, v185
	v_add_f32_e32 v97, v97, v186
	s_add_i32 s35, s62, 0x4800
	v_mfma_f32_32x32x16_bf16 v[64:79], a[212:215], a[180:183], v[64:79]
	ds_read_b64_tr_b16 v[108:109], v212 offset:0x3200
	v_add_f32_e32 v96, v96, v187
	v_add_f32_e32 v97, v97, v188
	s_mov_b32 s36, s16
	v_mfma_f32_32x32x16_bf16 v[48:63], a[244:247], a[148:151], v[48:63]
	ds_read_b64_tr_b16 v[110:111], v212 offset:0x3a00
	v_add_f32_e32 v96, v96, v189
	v_add_f32_e32 v97, v97, v190
	s_add_i32 s37, s62, 0x4c00
	v_mfma_f32_32x32x16_bf16 v[32:47], a[244:247], a[180:183], v[32:47]
	ds_read_b64_tr_b16 v[100:101], v212 offset:0x3400
	ds_read_b64_tr_b16 v[102:103], v212 offset:0x3c00
	v_add_f32_e32 v216, v96, v191
	v_add_f32_e32 v225, v97, v192
	s_mov_b32 s38, s2
	v_mfma_f32_32x32x16_bf16 v[80:95], a[216:219], a[152:155], v[80:95]
	ds_read_b64_tr_b16 v[96:97], v212 offset:0x3600
	v_cvt_pk_bf16_f32 v140, v141, v142
	v_add_f32_e32 v226, v233, v141
	v_add_f32_e32 v142, v234, v142
	v_mfma_f32_32x32x16_bf16 v[64:79], a[216:219], a[184:187], v[64:79]
	ds_read_b64_tr_b16 v[98:99], v212 offset:0x3e00
	v_cvt_pk_bf16_f32 v141, v143, v242
	v_add_f32_e32 v143, v226, v143
	v_add_f32_e32 v226, v142, v242
	v_mfma_f32_32x32x16_bf16 v[48:63], a[248:251], a[152:155], v[48:63]
	s_add_i32 s17, s29, 0x8400
	s_mov_b32 s39, s17
	v_cvt_pk_bf16_f32 v142, v243, v244
	v_add_f32_e32 v231, v143, v243
	v_add_f32_e32 v226, v226, v244
	v_mfma_f32_32x32x16_bf16 v[32:47], a[248:251], a[184:187], v[32:47]
	s_add_i32 s40, s62, 0x80
	v_cvt_pk_bf16_f32 v143, v245, v246
	v_add_f32_e32 v231, v231, v245
	v_add_f32_e32 v226, v226, v246
	v_mfma_f32_32x32x16_bf16 v[80:95], a[220:223], a[156:159], v[80:95]
	s_add_i32 s18, s29, 0x8800
	s_mov_b32 s41, s18
	v_add_f32_e32 v231, v231, v194
	v_add_f32_e32 v226, v226, v195
	v_mfma_f32_32x32x16_bf16 v[64:79], a[220:223], a[188:191], v[64:79]
	v_add_f32_e32 v231, v231, v215
	v_add_f32_e32 v226, v226, v224
	v_mfma_f32_32x32x16_bf16 v[48:63], a[252:255], a[156:159], v[48:63]
	s_add_i32 s19, s29, 0x8c00
	s_mov_b32 s42, s19
	v_add_f32_e32 v231, v231, v227
	v_add_f32_e32 v226, v226, v228
	v_mfma_f32_32x32x16_bf16 v[32:47], a[252:255], a[188:191], v[32:47]
	s_add_i32 s43, s62, 0x880
	v_add_f32_e32 v231, v231, v229
	v_add_f32_e32 v226, v226, v230
	v_add_f32_e32 v216, v216, v225
	s_waitcnt vmcnt(0) lgkmcnt(0)
	s_barrier
	v_mfma_f32_32x32x16_bf16 a[0:15], v[160:163], v[152:155], 0
	v_mov_b32_e32 v225, v216
	s_mov_b32 m0, s27
	s_nop 0
	buffer_load_dwordx4 v222, s[12:15], s30 offen lds
	v_mfma_f32_32x32x16_bf16 a[16:31], v[160:163], v[180:183], 0
	v_permlane32_swap_b32_e32 v216, v225
	v_add_f32_e32 v216, v216, v225
	s_mov_b32 m0, s31
	s_nop 0
	buffer_load_dwordx4 v223, s[12:15], s33 offen lds
	ds_read_b128 a[192:195], v218 offset:0
	v_mfma_f32_32x32x16_bf16 a[32:47], v[172:175], v[152:155], 0
	v_add_f32_e32 v225, v193, v216
	v_add_f32_e32 v216, v231, v226
	v_mov_b32_e32 v226, v216
	s_mov_b32 m0, s34
	s_nop 0
	buffer_load_dwordx4 v222, s[12:15], s35 offen lds
	ds_read_b128 a[196:199], v219 offset:0
	v_mfma_f32_32x32x16_bf16 a[48:63], v[172:175], v[180:183], 0
	v_permlane32_swap_b32_e32 v216, v226
	v_add_f32_e32 v216, v216, v226
	s_mov_b32 m0, s36
	s_nop 0
	buffer_load_dwordx4 v223, s[12:15], s37 offen lds
	ds_read_b128 a[200:203], v220 offset:0
	v_mfma_f32_32x32x16_bf16 a[64:79], v[168:171], v[152:155], 0
	v_add_f32_e32 v226, v193, v216
	s_mov_b32 m0, s38
	s_nop 0
	buffer_load_dwordx4 v196, s[4:7], s0 offen lds
	ds_read_b128 a[204:207], v221 offset:0
	v_mfma_f32_32x32x16_bf16 a[80:95], v[168:171], v[180:183], 0
	s_mov_b32 m0, s39
	s_nop 0
	buffer_load_dwordx4 v196, s[4:7], s40 offen lds
	ds_read_b128 a[208:211], v218 offset:128
	v_mfma_f32_32x32x16_bf16 a[96:111], v[176:179], v[152:155], 0
	s_mov_b32 m0, s41
	s_nop 0
	buffer_load_dwordx4 v196, s[4:7], s1 offen lds
	ds_read_b128 a[212:215], v219 offset:128
	v_mfma_f32_32x32x16_bf16 a[112:127], v[176:179], v[180:183], 0
	s_mov_b32 m0, s42
	s_nop 0
	buffer_load_dwordx4 v196, s[4:7], s43 offen lds
	ds_read_b128 a[216:219], v220 offset:128
	v_mfma_f32_32x32x16_bf16 a[0:15], v[164:167], v[128:131], a[0:15]
	ds_read_b128 a[220:223], v221 offset:128
	v_pk_add_f32 v[200:201], v[248:249], v[200:201]
	v_pk_add_f32 v[202:203], v[250:251], v[202:203]
	v_pk_add_f32 v[204:205], v[252:253], v[204:205]
	v_pk_add_f32 v[206:207], v[254:255], v[206:207]
	v_cvt_pk_bf16_f32 v248, v248, v249
	v_cvt_pk_bf16_f32 v249, v250, v251
	v_cvt_pk_bf16_f32 v250, v252, v253
	v_cvt_pk_bf16_f32 v251, v254, v255
	v_lshrrev_b32_e32 v252, 1, v208
	buffer_store_dwordx4 v[248:251], v252, s[4:7], s56 offen sc1
	s_add_i32 s56, s56, 0x1000
	s_nop 1
	global_load_dwordx4 v[248:251], v208, s[54:55] nt
	global_load_dwordx4 v[252:255], v208, s[54:55] offset:16 nt
	s_add_u32 s54, s54, 0x2000
	s_addc_u32 s55, s55, 0
	v_max3_f32 v152, v80, v81, v48
	v_max3_f32 v153, v82, v83, v49
	v_max3_f32 v152, v152, v50, v51
	v_mfma_f32_32x32x16_bf16 a[16:31], v[164:167], v[144:147], a[16:31]
	ds_read_b128 a[224:227], v218 offset:8192
	v_max3_f32 v152, v152, v84, v85
	v_max3_f32 v153, v153, v86, v87
	v_max3_f32 v152, v152, v52, v53
	v_max3_f32 v153, v153, v54, v55
	v_mfma_f32_32x32x16_bf16 a[32:47], v[156:159], v[128:131], a[32:47]
	ds_read_b128 a[228:231], v219 offset:8192
	v_max3_f32 v152, v152, v88, v89
	v_max3_f32 v153, v153, v90, v91
	v_max3_f32 v152, v152, v56, v57
	v_max3_f32 v153, v153, v58, v59
	v_mfma_f32_32x32x16_bf16 a[48:63], v[156:159], v[144:147], a[48:63]
	ds_read_b128 a[232:235], v220 offset:8192
	v_max3_f32 v152, v152, v92, v93
	v_max3_f32 v153, v153, v94, v95
	v_max3_f32 v152, v152, v60, v61
	v_max3_f32 v153, v153, v62, v63
	v_mfma_f32_32x32x16_bf16 a[64:79], v[148:151], v[128:131], a[64:79]
	ds_read_b128 a[236:239], v221 offset:8192
	v_max3_f32 v154, v64, v65, v32
	v_max3_f32 v155, v66, v67, v33
	v_max3_f32 v154, v154, v34, v35
	v_mfma_f32_32x32x16_bf16 a[80:95], v[148:151], v[144:147], a[80:95]
	ds_read_b128 a[240:243], v218 offset:8320
	v_max3_f32 v148, v154, v68, v69
	v_max3_f32 v149, v155, v70, v71
	v_max3_f32 v148, v148, v36, v37
	v_max3_f32 v149, v149, v38, v39
	v_mfma_f32_32x32x16_bf16 a[96:111], v[136:139], v[128:131], a[96:111]
	ds_read_b128 a[244:247], v219 offset:8320
	v_max3_f32 v128, v148, v72, v73
	v_max3_f32 v129, v149, v74, v75
	v_max3_f32 v128, v128, v40, v41
	v_max3_f32 v129, v129, v42, v43
	v_mfma_f32_32x32x16_bf16 a[112:127], v[136:139], v[144:147], a[112:127]
	ds_read_b128 a[248:251], v220 offset:8320
	v_max3_f32 v128, v128, v76, v77
	v_max3_f32 v129, v129, v78, v79
	v_max3_f32 v128, v128, v44, v45
	v_max3_f32 v130, v129, v46, v47
	v_mfma_f32_32x32x16_bf16 a[0:15], v[132:135], v[112:115], a[0:15]
	ds_read_b128 a[252:255], v221 offset:8320
	v_max_f32_e32 v129, v152, v153
	v_mov_b32_e32 v131, v129
	s_nop 1
	v_permlane32_swap_b32_e32 v129, v131
	v_max_f32_e32 v129, v129, v131
	v_mfma_f32_32x32x16_bf16 a[16:31], v[132:135], v[140:143], a[16:31]
	v_max_f32_e32 v128, v128, v130
	v_mov_b32_e32 v130, v128
	s_nop 1
	v_permlane32_swap_b32_e32 v128, v130
	v_max_f32_e32 v128, v128, v130
	v_max_f32_e32 v130, v129, v129
	v_max_f32_e32 v131, v128, v128
	v_max_f32_e32 v130, v130, v131
	s_mov_b32 s0, 0x41000000
	v_mfma_f32_32x32x16_bf16 a[32:47], v[124:127], v[112:115], a[32:47]
	v_cmp_lt_f32_e32 vcc, s0, v130
	s_cmp_lg_u64 vcc, 0
	s_cselect_b64 s[0:1], -1, 0
	s_cbranch_vccnz .LBB0_41
	v_mov_b32_e32 v216, 1.0

.LBB0_17:
	v_mfma_f32_32x32x16_bf16 v[112:127], a[192:195], a[128:131], v[0:15]
	v_exp_f32_e32 v48, v48
	v_exp_f32_e32 v49, v49
	ds_read_b64_tr_b16 v[172:173], v215 offset:0
	v_cvt_pk_bf16_f32 v164, v128, v129
	v_exp_f32_e32 v50, v50
	v_exp_f32_e32 v51, v51
	v_mfma_f32_32x32x16_bf16 v[96:111], a[192:195], a[160:163], v[16:31]
	ds_read_b64_tr_b16 v[174:175], v215 offset:0x800
	v_cvt_pk_bf16_f32 v165, v130, v131
	v_mfma_f32_32x32x16_bf16 v[80:95], a[224:227], a[128:131], v[0:15]
	ds_read_b64_tr_b16 v[184:185], v215 offset:0x200
	v_exp_f32_e32 v239, v52
	v_exp_f32_e32 v240, v53
	v_cvt_pk_bf16_f32 v166, v132, v133
	v_mfma_f32_32x32x16_bf16 v[64:79], a[224:227], a[160:163], v[16:31]
	ds_read_b64_tr_b16 v[186:187], v215 offset:0xa00
	ds_read_b64_tr_b16 v[180:181], v215 offset:0x400
	v_exp_f32_e32 v241, v54
	v_exp_f32_e32 v242, v55
	v_cvt_pk_bf16_f32 v167, v134, v135
	v_exp_f32_e32 v227, v56
	v_exp_f32_e32 v228, v57
	v_mfma_f32_32x32x16_bf16 v[112:127], a[196:199], a[132:135], v[112:127]
	ds_read_b64_tr_b16 v[182:183], v215 offset:0xc00
	v_cvt_pk_bf16_f32 v128, v136, v137
	v_exp_f32_e32 v229, v58
	v_exp_f32_e32 v230, v59
	v_mfma_f32_32x32x16_bf16 v[96:111], a[196:199], a[164:167], v[96:111]
	ds_read_b64_tr_b16 v[188:189], v215 offset:0x600
	v_cvt_pk_bf16_f32 v129, v138, v139
	v_exp_f32_e32 v231, v60
	v_exp_f32_e32 v232, v61
	v_mfma_f32_32x32x16_bf16 v[80:95], a[228:231], a[132:135], v[80:95]
	ds_read_b64_tr_b16 v[190:191], v215 offset:0xe00
	v_cvt_pk_bf16_f32 v130, v140, v141
	v_mfma_f32_32x32x16_bf16 v[64:79], a[228:231], a[164:167], v[64:79]
	ds_read_b64_tr_b16 v[176:177], v215 offset:0x1000
	v_exp_f32_e32 v233, v62
	v_exp_f32_e32 v234, v63
	ds_read_b64_tr_b16 v[178:179], v215 offset:0x1800
	v_cvt_pk_bf16_f32 v131, v142, v143
	v_exp_f32_e32 v141, v32
	v_exp_f32_e32 v142, v33
	v_mfma_f32_32x32x16_bf16 v[112:127], a[200:203], a[136:139], v[112:127]
	ds_read_b64_tr_b16 v[168:169], v215 offset:0x1200
	v_cvt_pk_bf16_f32 v192, v144, v145
	v_exp_f32_e32 v143, v34
	v_mfma_f32_32x32x16_bf16 v[96:111], a[200:203], a[168:171], v[96:111]
	ds_read_b64_tr_b16 v[170:171], v215 offset:0x1a00
	v_exp_f32_e32 v243, v35
	v_cvt_pk_bf16_f32 v193, v146, v147
	v_mfma_f32_32x32x16_bf16 v[80:95], a[232:235], a[136:139], v[80:95]
	ds_read_b64_tr_b16 v[160:161], v215 offset:0x1400
	v_exp_f32_e32 v244, v36
	v_exp_f32_e32 v245, v37
	v_cvt_pk_bf16_f32 v194, v148, v149
	v_mfma_f32_32x32x16_bf16 v[64:79], a[232:235], a[168:171], v[64:79]
	ds_read_b64_tr_b16 v[162:163], v215 offset:0x1c00
	ds_read_b64_tr_b16 v[136:137], v215 offset:0x1600
	v_exp_f32_e32 v246, v38
	v_exp_f32_e32 v247, v39
	v_cvt_pk_bf16_f32 v195, v150, v151
	v_exp_f32_e32 v148, v40
	v_exp_f32_e32 v149, v41
	v_mfma_f32_32x32x16_bf16 v[112:127], a[204:207], a[140:143], v[112:127]
	ds_read_b64_tr_b16 v[138:139], v215 offset:0x1e00
	v_cvt_pk_bf16_f32 v144, v152, v153
	v_exp_f32_e32 v150, v42
	v_exp_f32_e32 v151, v43
	v_mfma_f32_32x32x16_bf16 v[96:111], a[204:207], a[172:175], v[96:111]
	ds_read_b64_tr_b16 v[132:133], v215 offset:0x2000
	v_cvt_pk_bf16_f32 v145, v154, v155
	v_exp_f32_e32 v152, v44
	v_exp_f32_e32 v153, v45
	v_mfma_f32_32x32x16_bf16 v[80:95], a[236:239], a[140:143], v[80:95]
	ds_read_b64_tr_b16 v[134:135], v215 offset:0x2800
	v_cvt_pk_bf16_f32 v146, v156, v157
	v_mfma_f32_32x32x16_bf16 v[64:79], a[236:239], a[172:175], v[64:79]
	ds_read_b64_tr_b16 v[60:61], v215 offset:0x2200
	v_exp_f32_e32 v154, v46
	v_exp_f32_e32 v155, v47
	ds_read_b64_tr_b16 v[62:63], v215 offset:0x2a00
	v_cvt_pk_bf16_f32 v147, v158, v159
	s_mov_b32 s0, s29
	v_mfma_f32_32x32x16_bf16 v[112:127], a[208:211], a[144:147], v[112:127]
	ds_read_b64_tr_b16 v[56:57], v215 offset:0x2400
	v_cvt_pk_bf16_f32 v52, v48, v49
	v_add_f32_e32 v32, v236, v48
	v_add_f32_e32 v33, v235, v49
	s_add_i32 s57, s58, s59
	s_and_b32 s57, s57, 0x7ffff
	s_mov_b32 s33, s57
	s_mov_b32 s1, s33
	v_mfma_f32_32x32x16_bf16 v[96:111], a[208:211], a[176:179], v[96:111]
	ds_read_b64_tr_b16 v[58:59], v215 offset:0x2c00
	v_cvt_pk_bf16_f32 v53, v50, v51
	v_add_f32_e32 v32, v32, v50
	v_add_f32_e32 v33, v33, v51
	s_mov_b32 s35, s20
	v_mfma_f32_32x32x16_bf16 v[80:95], a[240:243], a[144:147], v[80:95]
	ds_read_b64_tr_b16 v[48:49], v215 offset:0x2600
	v_cvt_pk_bf16_f32 v54, v239, v240
	v_add_f32_e32 v32, v32, v239
	v_add_f32_e32 v33, v33, v240
	s_add_i32 s36, s57, 0x400
	v_mfma_f32_32x32x16_bf16 v[64:79], a[240:243], a[176:179], v[64:79]
	ds_read_b64_tr_b16 v[50:51], v215 offset:0x2e00
	ds_read_b64_tr_b16 v[44:45], v215 offset:0x3000
	v_cvt_pk_bf16_f32 v55, v241, v242
	v_add_f32_e32 v32, v32, v241
	v_add_f32_e32 v33, v33, v242
	s_mov_b32 s37, s21
	v_mfma_f32_32x32x16_bf16 v[112:127], a[212:215], a[148:151], v[112:127]
	ds_read_b64_tr_b16 v[46:47], v215 offset:0x3800
	v_add_f32_e32 v32, v32, v227
	v_add_f32_e32 v33, v33, v228
	s_add_i32 s34, s57, 0x800
	s_mov_b32 s38, s34
	v_mfma_f32_32x32x16_bf16 v[96:111], a[212:215], a[180:183], v[96:111]
	ds_read_b64_tr_b16 v[40:41], v215 offset:0x3200
	v_add_f32_e32 v32, v32, v229
	v_add_f32_e32 v33, v33, v230
	s_mov_b32 s39, s22
	v_mfma_f32_32x32x16_bf16 v[80:95], a[244:247], a[148:151], v[80:95]
	ds_read_b64_tr_b16 v[42:43], v215 offset:0x3a00
	v_add_f32_e32 v32, v32, v231
	v_add_f32_e32 v33, v33, v232
	s_add_i32 s40, s57, 0xc00
	v_mfma_f32_32x32x16_bf16 v[64:79], a[244:247], a[180:183], v[64:79]
	ds_read_b64_tr_b16 v[36:37], v215 offset:0x3400
	ds_read_b64_tr_b16 v[38:39], v215 offset:0x3c00
	v_add_f32_e32 v156, v32, v233
	v_add_f32_e32 v157, v33, v234
	s_mov_b32 s41, s23
	v_mfma_f32_32x32x16_bf16 v[112:127], a[216:219], a[152:155], v[112:127]
	ds_read_b64_tr_b16 v[32:33], v215 offset:0x3600
	v_cvt_pk_bf16_f32 v140, v141, v142
	v_add_f32_e32 v158, v237, v141
	v_add_f32_e32 v142, v238, v142
	s_mov_b32 s42, s58
	v_mfma_f32_32x32x16_bf16 v[96:111], a[216:219], a[184:187], v[96:111]
	ds_read_b64_tr_b16 v[34:35], v215 offset:0x3e00
	v_cvt_pk_bf16_f32 v141, v143, v243
	v_add_f32_e32 v143, v158, v143
	v_add_f32_e32 v158, v142, v243
	v_mfma_f32_32x32x16_bf16 v[80:95], a[248:251], a[152:155], v[80:95]
	s_mov_b32 s43, s24
	v_cvt_pk_bf16_f32 v142, v244, v245
	v_add_f32_e32 v159, v143, v244
	v_add_f32_e32 v158, v158, v245
	v_mfma_f32_32x32x16_bf16 v[64:79], a[248:251], a[184:187], v[64:79]
	s_add_i32 s44, s58, 0x80
	v_cvt_pk_bf16_f32 v143, v246, v247
	v_add_f32_e32 v159, v159, v246
	v_add_f32_e32 v158, v158, v247
	v_mfma_f32_32x32x16_bf16 v[112:127], a[220:223], a[156:159], v[112:127]
	s_mov_b32 s45, s25
	v_add_f32_e32 v159, v159, v148
	v_add_f32_e32 v158, v158, v149
	v_mfma_f32_32x32x16_bf16 v[96:111], a[220:223], a[188:191], v[96:111]
	s_add_i32 s46, s58, 0x800
	v_add_f32_e32 v159, v159, v150
	v_add_f32_e32 v158, v158, v151
	v_mfma_f32_32x32x16_bf16 v[80:95], a[252:255], a[156:159], v[80:95]
	s_mov_b32 s47, s26
	v_add_f32_e32 v159, v159, v152
	v_add_f32_e32 v158, v158, v153
	v_mfma_f32_32x32x16_bf16 v[64:79], a[252:255], a[188:191], v[64:79]
	s_add_i32 s48, s58, 0x880
	v_add_f32_e32 v159, v159, v154
	v_add_f32_e32 v158, v158, v155
	v_add_f32_e32 v156, v156, v157
	s_waitcnt vmcnt(0) lgkmcnt(0)
	s_barrier
	v_mfma_f32_32x32x16_bf16 a[0:15], v[172:175], v[164:167], a[0:15]
	v_mov_b32_e32 v157, v156
	s_mov_b32 m0, s0
	s_nop 0
	buffer_load_dwordx4 v222, s[12:15], s1 offen lds
	v_mfma_f32_32x32x16_bf16 a[16:31], v[172:175], v[192:195], a[16:31]
	v_permlane32_swap_b32_e32 v156, v157
	v_add_f32_e32 v156, v156, v157
	s_mov_b32 m0, s35
	s_nop 0
	buffer_load_dwordx4 v223, s[12:15], s36 offen lds
	ds_read_b128 a[192:195], v217 offset:0
	v_mfma_f32_32x32x16_bf16 a[32:47], v[184:187], v[164:167], a[32:47]
	v_add_f32_e32 v225, v225, v156
	v_add_f32_e32 v156, v159, v158
	v_mov_b32_e32 v157, v156
	s_mov_b32 m0, s37
	s_nop 0
	buffer_load_dwordx4 v222, s[12:15], s38 offen lds
	ds_read_b128 a[196:199], v199 offset:0
	v_mfma_f32_32x32x16_bf16 a[48:63], v[184:187], v[192:195], a[48:63]
	v_permlane32_swap_b32_e32 v156, v157
	v_add_f32_e32 v156, v156, v157
	s_mov_b32 m0, s39
	s_nop 0
	buffer_load_dwordx4 v223, s[12:15], s40 offen lds
	ds_read_b128 a[200:203], v198 offset:0
	v_mfma_f32_32x32x16_bf16 a[64:79], v[180:183], v[164:167], a[64:79]
	v_add_f32_e32 v226, v226, v156
	s_mov_b32 m0, s41
	s_nop 0
	buffer_load_dwordx4 v196, s[4:7], s42 offen lds
	ds_read_b128 a[204:207], v197 offset:0
	v_mfma_f32_32x32x16_bf16 a[80:95], v[180:183], v[192:195], a[80:95]
	s_mov_b32 m0, s43
	s_nop 0
	buffer_load_dwordx4 v196, s[4:7], s44 offen lds
	ds_read_b128 a[208:211], v217 offset:128
	v_mfma_f32_32x32x16_bf16 a[96:111], v[188:191], v[164:167], a[96:111]
	s_mov_b32 m0, s45
	s_nop 0
	buffer_load_dwordx4 v196, s[4:7], s46 offen lds
	ds_read_b128 a[212:215], v199 offset:128
	v_mfma_f32_32x32x16_bf16 a[112:127], v[188:191], v[192:195], a[112:127]
	s_mov_b32 m0, s47
	s_nop 0
	buffer_load_dwordx4 v196, s[4:7], s48 offen lds
	ds_read_b128 a[216:219], v198 offset:128
	s_nop 0
	v_mfma_f32_32x32x16_bf16 a[0:15], v[176:179], v[128:131], a[0:15]
	ds_read_b128 a[220:223], v197 offset:128
	s_cmp_gt_u32 s27, 12
	s_cbranch_scc1 .Lkc_skip_a
	v_cvt_pk_bf16_f32 v248, v248, v249
	v_cvt_pk_bf16_f32 v249, v250, v251
	v_cvt_pk_bf16_f32 v250, v252, v253
	v_cvt_pk_bf16_f32 v251, v254, v255
	v_lshrrev_b32_e32 v252, 1, v208
	buffer_store_dwordx4 v[248:251], v252, s[12:15], s56 offen sc1
	s_nop 1
	global_load_dwordx4 v[248:251], v208, s[74:75] nt
	global_load_dwordx4 v[252:255], v208, s[74:75] offset:16 nt
	s_add_u32 s74, s74, 0x2000
	s_addc_u32 s75, s75, 0

.LBB0_19:
	s_waitcnt lgkmcnt(0)
	v_mfma_f32_32x32x16_bf16 v[112:127], a[192:195], a[128:131], v[0:15]
	v_exp_f32_e32 v80, v80
	v_exp_f32_e32 v81, v81
	ds_read_b64_tr_b16 v[180:181], v212 offset:0
	v_cvt_pk_bf16_f32 v168, v128, v129
	v_exp_f32_e32 v82, v82
	v_exp_f32_e32 v83, v83
	v_mfma_f32_32x32x16_bf16 v[96:111], a[192:195], a[160:163], v[16:31]
	ds_read_b64_tr_b16 v[182:183], v212 offset:0x800
	v_cvt_pk_bf16_f32 v169, v130, v131
	v_mfma_f32_32x32x16_bf16 v[48:63], a[224:227], a[128:131], v[0:15]
	ds_read_b64_tr_b16 v[184:185], v212 offset:0x200
	v_exp_f32_e32 v239, v84
	v_exp_f32_e32 v240, v85
	v_cvt_pk_bf16_f32 v170, v132, v133
	v_mfma_f32_32x32x16_bf16 v[32:47], a[224:227], a[160:163], v[16:31]
	ds_read_b64_tr_b16 v[186:187], v212 offset:0xa00
	ds_read_b64_tr_b16 v[176:177], v212 offset:0x400
	v_exp_f32_e32 v241, v86
	v_exp_f32_e32 v242, v87
	v_cvt_pk_bf16_f32 v171, v134, v135
	v_exp_f32_e32 v227, v88
	v_exp_f32_e32 v228, v89
	v_mfma_f32_32x32x16_bf16 v[112:127], a[196:199], a[132:135], v[112:127]
	ds_read_b64_tr_b16 v[178:179], v212 offset:0xc00
	v_cvt_pk_bf16_f32 v128, v136, v137
	v_exp_f32_e32 v229, v90
	v_exp_f32_e32 v230, v91
	v_mfma_f32_32x32x16_bf16 v[96:111], a[196:199], a[164:167], v[96:111]
	ds_read_b64_tr_b16 v[188:189], v212 offset:0x600
	v_cvt_pk_bf16_f32 v129, v138, v139
	v_exp_f32_e32 v231, v92
	v_exp_f32_e32 v232, v93
	v_mfma_f32_32x32x16_bf16 v[48:63], a[228:231], a[132:135], v[48:63]
	ds_read_b64_tr_b16 v[190:191], v212 offset:0xe00
	v_cvt_pk_bf16_f32 v130, v140, v141
	v_mfma_f32_32x32x16_bf16 v[32:47], a[228:231], a[164:167], v[32:47]
	ds_read_b64_tr_b16 v[172:173], v212 offset:0x1000
	v_exp_f32_e32 v233, v94
	v_exp_f32_e32 v234, v95
	ds_read_b64_tr_b16 v[174:175], v212 offset:0x1800
	v_cvt_pk_bf16_f32 v131, v142, v143
	v_exp_f32_e32 v141, v64
	v_exp_f32_e32 v142, v65
	v_mfma_f32_32x32x16_bf16 v[112:127], a[200:203], a[136:139], v[112:127]
	ds_read_b64_tr_b16 v[164:165], v212 offset:0x1200
	v_cvt_pk_bf16_f32 v192, v144, v145
	v_exp_f32_e32 v143, v66
	v_mfma_f32_32x32x16_bf16 v[96:111], a[200:203], a[168:171], v[96:111]
	ds_read_b64_tr_b16 v[166:167], v212 offset:0x1a00
	v_exp_f32_e32 v243, v67
	v_cvt_pk_bf16_f32 v193, v146, v147
	v_mfma_f32_32x32x16_bf16 v[48:63], a[232:235], a[136:139], v[48:63]
	ds_read_b64_tr_b16 v[160:161], v212 offset:0x1400
	v_exp_f32_e32 v244, v68
	v_exp_f32_e32 v245, v69
	v_cvt_pk_bf16_f32 v194, v148, v149
	v_mfma_f32_32x32x16_bf16 v[32:47], a[232:235], a[168:171], v[32:47]
	ds_read_b64_tr_b16 v[162:163], v212 offset:0x1c00
	ds_read_b64_tr_b16 v[136:137], v212 offset:0x1600
	v_exp_f32_e32 v246, v70
	v_exp_f32_e32 v247, v71
	v_cvt_pk_bf16_f32 v195, v150, v151
	v_exp_f32_e32 v148, v72
	v_exp_f32_e32 v149, v73
	v_mfma_f32_32x32x16_bf16 v[112:127], a[204:207], a[140:143], v[112:127]
	ds_read_b64_tr_b16 v[138:139], v212 offset:0x1e00
	v_cvt_pk_bf16_f32 v144, v152, v153
	v_exp_f32_e32 v150, v74
	v_exp_f32_e32 v151, v75
	v_mfma_f32_32x32x16_bf16 v[96:111], a[204:207], a[172:175], v[96:111]
	ds_read_b64_tr_b16 v[132:133], v212 offset:0x2000
	v_cvt_pk_bf16_f32 v145, v154, v155
	v_exp_f32_e32 v152, v76
	v_exp_f32_e32 v153, v77
	v_mfma_f32_32x32x16_bf16 v[48:63], a[236:239], a[140:143], v[48:63]
	ds_read_b64_tr_b16 v[134:135], v212 offset:0x2800
	v_cvt_pk_bf16_f32 v146, v156, v157
	v_mfma_f32_32x32x16_bf16 v[32:47], a[236:239], a[172:175], v[32:47]
	ds_read_b64_tr_b16 v[92:93], v212 offset:0x2200
	v_exp_f32_e32 v154, v78
	v_exp_f32_e32 v155, v79
	ds_read_b64_tr_b16 v[94:95], v212 offset:0x2a00
	v_cvt_pk_bf16_f32 v147, v158, v159
	s_mov_b32 s0, s3
	v_mfma_f32_32x32x16_bf16 v[112:127], a[208:211], a[144:147], v[112:127]
	ds_read_b64_tr_b16 v[88:89], v212 offset:0x2400
	v_cvt_pk_bf16_f32 v84, v80, v81
	v_add_f32_e32 v64, v236, v80
	v_add_f32_e32 v65, v235, v81
	s_add_i32 s58, s57, s60
	s_and_b32 s58, s58, 0x7ffff
	s_mov_b32 s1, s58
	v_mfma_f32_32x32x16_bf16 v[96:111], a[208:211], a[176:179], v[96:111]
	ds_read_b64_tr_b16 v[90:91], v212 offset:0x2c00
	v_cvt_pk_bf16_f32 v85, v82, v83
	v_add_f32_e32 v64, v64, v82
	v_add_f32_e32 v65, v65, v83
	s_mov_b32 s35, s10
	v_mfma_f32_32x32x16_bf16 v[48:63], a[240:243], a[144:147], v[48:63]
	ds_read_b64_tr_b16 v[80:81], v212 offset:0x2600
	v_cvt_pk_bf16_f32 v86, v239, v240
	v_add_f32_e32 v64, v64, v239
	v_add_f32_e32 v65, v65, v240
	s_add_i32 s36, s58, 0x400
	v_mfma_f32_32x32x16_bf16 v[32:47], a[240:243], a[176:179], v[32:47]
	ds_read_b64_tr_b16 v[82:83], v212 offset:0x2e00
	ds_read_b64_tr_b16 v[76:77], v212 offset:0x3000
	v_cvt_pk_bf16_f32 v87, v241, v242
	v_add_f32_e32 v64, v64, v241
	v_add_f32_e32 v65, v65, v242
	s_mov_b32 s37, s11
	v_mfma_f32_32x32x16_bf16 v[112:127], a[212:215], a[148:151], v[112:127]
	ds_read_b64_tr_b16 v[78:79], v212 offset:0x3800
	v_add_f32_e32 v64, v64, v227
	v_add_f32_e32 v65, v65, v228
	s_add_i32 s38, s58, 0x800
	v_mfma_f32_32x32x16_bf16 v[96:111], a[212:215], a[180:183], v[96:111]
	ds_read_b64_tr_b16 v[72:73], v212 offset:0x3200
	v_add_f32_e32 v64, v64, v229
	v_add_f32_e32 v65, v65, v230
	s_mov_b32 s39, s16
	v_mfma_f32_32x32x16_bf16 v[48:63], a[244:247], a[148:151], v[48:63]
	ds_read_b64_tr_b16 v[74:75], v212 offset:0x3a00
	v_add_f32_e32 v64, v64, v231
	v_add_f32_e32 v65, v65, v232
	s_add_i32 s40, s58, 0xc00
	v_mfma_f32_32x32x16_bf16 v[32:47], a[244:247], a[180:183], v[32:47]
	ds_read_b64_tr_b16 v[68:69], v212 offset:0x3400
	ds_read_b64_tr_b16 v[70:71], v212 offset:0x3c00
	v_add_f32_e32 v156, v64, v233
	v_add_f32_e32 v157, v65, v234
	s_mov_b32 s41, s2
	v_mfma_f32_32x32x16_bf16 v[112:127], a[216:219], a[152:155], v[112:127]
	ds_read_b64_tr_b16 v[64:65], v212 offset:0x3600
	v_cvt_pk_bf16_f32 v140, v141, v142
	v_add_f32_e32 v158, v237, v141
	v_add_f32_e32 v142, v238, v142
	v_mfma_f32_32x32x16_bf16 v[96:111], a[216:219], a[184:187], v[96:111]
	ds_read_b64_tr_b16 v[66:67], v212 offset:0x3e00
	v_cvt_pk_bf16_f32 v141, v143, v243
	v_add_f32_e32 v143, v158, v143
	v_add_f32_e32 v158, v142, v243
	v_mfma_f32_32x32x16_bf16 v[48:63], a[248:251], a[152:155], v[48:63]
	s_mov_b32 s42, s17
	v_cvt_pk_bf16_f32 v142, v244, v245
	v_add_f32_e32 v159, v143, v244
	v_add_f32_e32 v158, v158, v245
	v_mfma_f32_32x32x16_bf16 v[32:47], a[248:251], a[184:187], v[32:47]
	s_add_i32 s43, s57, 0x80
	v_cvt_pk_bf16_f32 v143, v246, v247
	v_add_f32_e32 v159, v159, v246
	v_add_f32_e32 v158, v158, v247
	v_mfma_f32_32x32x16_bf16 v[112:127], a[220:223], a[156:159], v[112:127]
	s_mov_b32 s44, s18
	v_add_f32_e32 v159, v159, v148
	v_add_f32_e32 v158, v158, v149
	v_mfma_f32_32x32x16_bf16 v[96:111], a[220:223], a[188:191], v[96:111]
	v_add_f32_e32 v159, v159, v150
	v_add_f32_e32 v158, v158, v151
	v_mfma_f32_32x32x16_bf16 v[48:63], a[252:255], a[156:159], v[48:63]
	s_mov_b32 s45, s19
	v_add_f32_e32 v159, v159, v152
	v_add_f32_e32 v158, v158, v153
	v_mfma_f32_32x32x16_bf16 v[32:47], a[252:255], a[188:191], v[32:47]
	s_add_i32 s46, s57, 0x880
	v_add_f32_e32 v159, v159, v154
	v_add_f32_e32 v158, v158, v155
	v_add_f32_e32 v156, v156, v157
	s_waitcnt vmcnt(0) lgkmcnt(0)
	s_barrier
	v_mfma_f32_32x32x16_bf16 a[0:15], v[180:183], v[168:171], a[0:15]
	v_mov_b32_e32 v157, v156
	s_mov_b32 m0, s0
	s_nop 0
	buffer_load_dwordx4 v222, s[12:15], s1 offen lds
	v_mfma_f32_32x32x16_bf16 a[16:31], v[180:183], v[192:195], a[16:31]
	v_permlane32_swap_b32_e32 v156, v157
	v_add_f32_e32 v156, v156, v157
	s_mov_b32 m0, s35
	s_nop 0
	buffer_load_dwordx4 v223, s[12:15], s36 offen lds
	ds_read_b128 a[192:195], v218 offset:0
	v_mfma_f32_32x32x16_bf16 a[32:47], v[184:187], v[168:171], a[32:47]
	v_add_f32_e32 v225, v225, v156
	v_add_f32_e32 v156, v159, v158
	v_mov_b32_e32 v157, v156
	s_mov_b32 m0, s37
	s_nop 0
	buffer_load_dwordx4 v222, s[12:15], s38 offen lds
	ds_read_b128 a[196:199], v219 offset:0
	v_mfma_f32_32x32x16_bf16 a[48:63], v[184:187], v[192:195], a[48:63]
	v_permlane32_swap_b32_e32 v156, v157
	v_add_f32_e32 v156, v156, v157
	s_mov_b32 m0, s39
	s_nop 0
	buffer_load_dwordx4 v223, s[12:15], s40 offen lds
	ds_read_b128 a[200:203], v220 offset:0
	v_mfma_f32_32x32x16_bf16 a[64:79], v[176:179], v[168:171], a[64:79]
	v_add_f32_e32 v226, v226, v156
	s_mov_b32 m0, s41
	s_nop 0
	buffer_load_dwordx4 v196, s[4:7], s33 offen lds
	ds_read_b128 a[204:207], v221 offset:0
	v_mfma_f32_32x32x16_bf16 a[80:95], v[176:179], v[192:195], a[80:95]
	s_mov_b32 m0, s42
	s_nop 0
	buffer_load_dwordx4 v196, s[4:7], s43 offen lds
	ds_read_b128 a[208:211], v218 offset:128
	v_mfma_f32_32x32x16_bf16 a[96:111], v[188:191], v[168:171], a[96:111]
	s_mov_b32 m0, s44
	s_nop 0
	buffer_load_dwordx4 v196, s[4:7], s34 offen lds
	ds_read_b128 a[212:215], v219 offset:128
	v_mfma_f32_32x32x16_bf16 a[112:127], v[188:191], v[192:195], a[112:127]
	s_mov_b32 m0, s45
	s_nop 0
	buffer_load_dwordx4 v196, s[4:7], s46 offen lds
	ds_read_b128 a[216:219], v220 offset:128
	s_nop 0
	v_mfma_f32_32x32x16_bf16 a[0:15], v[172:175], v[128:131], a[0:15]
	ds_read_b128 a[220:223], v221 offset:128
	s_cmp_gt_u32 s27, 12
	s_cbranch_scc1 .Lkc_skip_b
	v_pk_add_f32 v[200:201], v[248:249], v[200:201]
	v_pk_add_f32 v[202:203], v[250:251], v[202:203]
	v_pk_add_f32 v[204:205], v[252:253], v[204:205]
	v_pk_add_f32 v[206:207], v[254:255], v[206:207]
	v_cvt_pk_bf16_f32 v248, v248, v249
	v_cvt_pk_bf16_f32 v249, v250, v251
	v_cvt_pk_bf16_f32 v250, v252, v253
	v_cvt_pk_bf16_f32 v251, v254, v255
	v_lshrrev_b32_e32 v252, 1, v208
	buffer_store_dwordx4 v[248:251], v252, s[4:7], s56 offen sc1
	s_add_i32 s56, s56, 0x1000
	s_cmp_gt_u32 s27, 10
	s_cbranch_scc1 .Lkc_skip_b
	s_nop 1
	global_load_dwordx4 v[248:251], v208, s[54:55] nt
	global_load_dwordx4 v[252:255], v208, s[54:55] offset:16 nt
	s_add_u32 s54, s54, 0x2000
	s_addc_u32 s55, s55, 0

.LBB0_36:
	s_lshl_b32 s53, s50, 6
	s_add_i32 s53, s53, s52
	v_mov_b32_e32 v200, s53
	s_lshl_b32 s53, s50, 14
	s_add_i32 s53, s53, 0x10000
	v_mov_b32_e32 v201, s53
	v_mbcnt_lo_u32_b32 v204, -1, 0
	v_mbcnt_hi_u32_b32 v204, -1, v204
	v_lshrrev_b32_e32 v202, 4, v204
	v_add_u32_e32 v203, 4, v202
	v_add_u32_e32 v205, 8, v202
	v_add_u32_e32 v206, 12, v202
	v_add_u32_e32 v207, 16, v202
	v_add_u32_e32 v208, 20, v202
	v_add_u32_e32 v209, 24, v202
	v_add_u32_e32 v210, 28, v202
	v_mfma_f32_32x32x16_bf16 v[112:127], a[192:195], a[128:131], v[0:15]
	v_exp_f32_e32 v48, v48
	v_exp_f32_e32 v49, v49
	ds_read_b64_tr_b16 v[180:181], v215 offset:0
	v_cvt_pk_bf16_f32 v164, v128, v129
	v_exp_f32_e32 v50, v50
	v_exp_f32_e32 v51, v51
	v_mfma_f32_32x32x16_bf16 v[96:111], a[192:195], a[160:163], v[16:31]
	ds_read_b64_tr_b16 v[182:183], v215 offset:0x800
	v_cvt_pk_bf16_f32 v165, v130, v131
	v_mfma_f32_32x32x16_bf16 v[80:95], a[224:227], a[128:131], v[0:15]
	v_exp_f32_e32 v218, v52
	v_exp_f32_e32 v219, v53
	ds_read_b64_tr_b16 v[188:189], v215 offset:0x200
	v_cvt_pk_bf16_f32 v166, v132, v133
	v_mfma_f32_32x32x16_bf16 v[64:79], a[224:227], a[160:163], v[16:31]
	ds_read_b64_tr_b16 v[190:191], v215 offset:0xa00
	ds_read_b64_tr_b16 v[176:177], v215 offset:0x400
	v_exp_f32_e32 v230, v54
	v_exp_f32_e32 v231, v55
	v_cvt_pk_bf16_f32 v167, v134, v135
	v_exp_f32_e32 v220, v56
	v_exp_f32_e32 v221, v57
	v_mfma_f32_32x32x16_bf16 v[112:127], a[196:199], a[132:135], v[112:127]
	ds_read_b64_tr_b16 v[178:179], v215 offset:0xc00
	v_cvt_pk_bf16_f32 v128, v136, v137
	v_exp_f32_e32 v222, v58
	v_exp_f32_e32 v223, v59
	v_mfma_f32_32x32x16_bf16 v[96:111], a[196:199], a[164:167], v[96:111]
	ds_read_b64_tr_b16 v[184:185], v215 offset:0x600
	v_cvt_pk_bf16_f32 v129, v138, v139
	v_exp_f32_e32 v224, v60
	v_exp_f32_e32 v227, v61
	v_mfma_f32_32x32x16_bf16 v[80:95], a[228:231], a[132:135], v[80:95]
	ds_read_b64_tr_b16 v[186:187], v215 offset:0xe00
	v_cvt_pk_bf16_f32 v130, v140, v141
	v_mfma_f32_32x32x16_bf16 v[64:79], a[228:231], a[164:167], v[64:79]
	ds_read_b64_tr_b16 v[172:173], v215 offset:0x1000
	v_exp_f32_e32 v228, v62
	v_exp_f32_e32 v229, v63
	ds_read_b64_tr_b16 v[174:175], v215 offset:0x1800
	v_cvt_pk_bf16_f32 v131, v142, v143
	v_exp_f32_e32 v141, v32
	v_exp_f32_e32 v142, v33
	v_mfma_f32_32x32x16_bf16 v[112:127], a[200:203], a[136:139], v[112:127]
	ds_read_b64_tr_b16 v[168:169], v215 offset:0x1200
	v_cvt_pk_bf16_f32 v192, v144, v145
	v_exp_f32_e32 v143, v34
	v_mfma_f32_32x32x16_bf16 v[96:111], a[200:203], a[168:171], v[96:111]
	ds_read_b64_tr_b16 v[170:171], v215 offset:0x1a00
	v_exp_f32_e32 v232, v35
	v_cvt_pk_bf16_f32 v193, v146, v147
	v_mfma_f32_32x32x16_bf16 v[80:95], a[232:235], a[136:139], v[80:95]
	ds_read_b64_tr_b16 v[160:161], v215 offset:0x1400
	v_exp_f32_e32 v233, v36
	v_exp_f32_e32 v234, v37
	v_cvt_pk_bf16_f32 v194, v148, v149
	v_mfma_f32_32x32x16_bf16 v[64:79], a[232:235], a[168:171], v[64:79]
	ds_read_b64_tr_b16 v[162:163], v215 offset:0x1c00
	ds_read_b64_tr_b16 v[136:137], v215 offset:0x1600
	v_exp_f32_e32 v239, v38
	v_exp_f32_e32 v240, v39
	v_cvt_pk_bf16_f32 v195, v150, v151
	v_exp_f32_e32 v148, v40
	v_exp_f32_e32 v149, v41
	v_mfma_f32_32x32x16_bf16 v[112:127], a[204:207], a[140:143], v[112:127]
	ds_read_b64_tr_b16 v[138:139], v215 offset:0x1e00
	v_cvt_pk_bf16_f32 v144, v152, v153
	v_exp_f32_e32 v150, v42
	v_exp_f32_e32 v151, v43
	v_mfma_f32_32x32x16_bf16 v[96:111], a[204:207], a[172:175], v[96:111]
	ds_read_b64_tr_b16 v[132:133], v215 offset:0x2000
	v_cvt_pk_bf16_f32 v145, v154, v155
	v_exp_f32_e32 v152, v44
	v_exp_f32_e32 v153, v45
	v_mfma_f32_32x32x16_bf16 v[80:95], a[236:239], a[140:143], v[80:95]
	ds_read_b64_tr_b16 v[134:135], v215 offset:0x2800
	v_cvt_pk_bf16_f32 v146, v156, v157
	v_mfma_f32_32x32x16_bf16 v[64:79], a[236:239], a[172:175], v[64:79]
	ds_read_b64_tr_b16 v[60:61], v215 offset:0x2200
	v_exp_f32_e32 v154, v46
	v_exp_f32_e32 v155, v47
	ds_read_b64_tr_b16 v[62:63], v215 offset:0x2a00
	v_cvt_pk_bf16_f32 v147, v158, v159
	v_mfma_f32_32x32x16_bf16 v[112:127], a[208:211], a[144:147], v[112:127]
	ds_read_b64_tr_b16 v[56:57], v215 offset:0x2400
	v_cvt_pk_bf16_f32 v52, v48, v49
	v_add_f32_e32 v32, v236, v48
	v_add_f32_e32 v33, v235, v49
	s_add_i32 s12, s28, 0x80000
	s_mov_b32 s0, s12
	v_mfma_f32_32x32x16_bf16 v[96:111], a[208:211], a[176:179], v[96:111]
	ds_read_b64_tr_b16 v[58:59], v215 offset:0x2c00
	v_cvt_pk_bf16_f32 v53, v50, v51
	v_add_f32_e32 v32, v32, v50
	v_add_f32_e32 v33, v33, v51
	v_mfma_f32_32x32x16_bf16 v[80:95], a[240:243], a[144:147], v[80:95]
	ds_read_b64_tr_b16 v[48:49], v215 offset:0x2600
	v_cvt_pk_bf16_f32 v54, v218, v219
	v_add_f32_e32 v32, v32, v218
	v_add_f32_e32 v33, v33, v219
	s_add_i32 s1, s28, 0x80400
	v_mfma_f32_32x32x16_bf16 v[64:79], a[240:243], a[176:179], v[64:79]
	ds_read_b64_tr_b16 v[50:51], v215 offset:0x2e00
	ds_read_b64_tr_b16 v[44:45], v215 offset:0x3000
	v_cvt_pk_bf16_f32 v55, v230, v231
	v_add_f32_e32 v32, v32, v230
	v_add_f32_e32 v33, v33, v231
	v_mfma_f32_32x32x16_bf16 v[112:127], a[212:215], a[148:151], v[112:127]
	ds_read_b64_tr_b16 v[46:47], v215 offset:0x3800
	v_add_f32_e32 v32, v32, v220
	v_add_f32_e32 v33, v33, v221
	s_add_i32 s13, s28, 0x80800
	s_mov_b32 s14, s13
	v_mfma_f32_32x32x16_bf16 v[96:111], a[212:215], a[180:183], v[96:111]
	ds_read_b64_tr_b16 v[40:41], v215 offset:0x3200
	v_add_f32_e32 v32, v32, v222
	v_add_f32_e32 v33, v33, v223
	v_mfma_f32_32x32x16_bf16 v[80:95], a[244:247], a[148:151], v[80:95]
	ds_read_b64_tr_b16 v[42:43], v215 offset:0x3a00
	v_add_f32_e32 v32, v32, v224
	v_add_f32_e32 v33, v33, v227
	s_add_i32 s15, s28, 0x80c00
	v_mfma_f32_32x32x16_bf16 v[64:79], a[244:247], a[180:183], v[64:79]
	ds_read_b64_tr_b16 v[36:37], v215 offset:0x3400
	ds_read_b64_tr_b16 v[38:39], v215 offset:0x3c00
	v_add_f32_e32 v156, v32, v228
	v_add_f32_e32 v157, v33, v229
	v_mfma_f32_32x32x16_bf16 v[112:127], a[216:219], a[152:155], v[112:127]
	ds_read_b64_tr_b16 v[32:33], v215 offset:0x3600
	v_cvt_pk_bf16_f32 v140, v141, v142
	v_add_f32_e32 v158, v237, v141
	v_add_f32_e32 v142, v238, v142
	s_add_i32 s27, s63, 0x0
	v_mfma_f32_32x32x16_bf16 v[96:111], a[216:219], a[184:187], v[96:111]
	ds_read_b64_tr_b16 v[34:35], v215 offset:0x3e00
	v_cvt_pk_bf16_f32 v141, v143, v232
	v_add_f32_e32 v143, v158, v143
	v_add_f32_e32 v158, v142, v232
	v_mfma_f32_32x32x16_bf16 v[80:95], a[248:251], a[152:155], v[80:95]
	v_cvt_pk_bf16_f32 v142, v233, v234
	v_add_f32_e32 v159, v143, v233
	v_add_f32_e32 v158, v158, v234
	v_mfma_f32_32x32x16_bf16 v[64:79], a[248:251], a[184:187], v[64:79]
	s_add_i32 s30, s63, 0x80
	v_cvt_pk_bf16_f32 v143, v239, v240
	v_add_f32_e32 v159, v159, v239
	v_add_f32_e32 v158, v158, v240
	v_mfma_f32_32x32x16_bf16 v[112:127], a[220:223], a[156:159], v[112:127]
	v_add_f32_e32 v159, v159, v148
	v_add_f32_e32 v158, v158, v149
	v_mfma_f32_32x32x16_bf16 v[96:111], a[220:223], a[188:191], v[96:111]
	s_add_i32 s31, s63, 0x800
	v_add_f32_e32 v159, v159, v150
	v_add_f32_e32 v158, v158, v151
	v_mfma_f32_32x32x16_bf16 v[80:95], a[252:255], a[156:159], v[80:95]
	v_add_f32_e32 v159, v159, v152
	v_add_f32_e32 v158, v158, v153
	v_mfma_f32_32x32x16_bf16 v[64:79], a[252:255], a[188:191], v[64:79]
	s_add_i32 s33, s63, 0x880
	v_add_f32_e32 v159, v159, v154
	v_add_f32_e32 v158, v158, v155
	v_add_f32_e32 v156, v156, v157
	s_waitcnt vmcnt(0) lgkmcnt(0)
	s_barrier
	v_mfma_f32_32x32x16_bf16 a[0:15], v[180:183], v[164:167], a[0:15]
	v_mov_b32_e32 v157, v156
	v_mfma_f32_32x32x16_bf16 a[16:31], v[180:183], v[192:195], a[16:31]
	s_nop 1
	v_permlane32_swap_b32_e32 v156, v157
	v_add_f32_e32 v156, v156, v157
	ds_read_b128 a[192:195], v217 offset:0
	v_mfma_f32_32x32x16_bf16 a[32:47], v[188:191], v[164:167], a[32:47]
	v_add_f32_e32 v219, v225, v156
	v_add_f32_e32 v156, v159, v158
	v_mov_b32_e32 v157, v156
	ds_read_b128 a[196:199], v199 offset:0
	v_mfma_f32_32x32x16_bf16 a[48:63], v[188:191], v[192:195], a[48:63]
	v_permlane32_swap_b32_e32 v156, v157
	v_add_f32_e32 v156, v156, v157
	ds_read_b128 a[200:203], v198 offset:0
	v_mfma_f32_32x32x16_bf16 a[64:79], v[176:179], v[164:167], a[64:79]
	v_add_f32_e32 v218, v226, v156
	s_mov_b32 m0, s23
	s_nop 0
	buffer_load_dwordx4 v196, s[4:7], s27 offen lds
	ds_read_b128 a[204:207], v197 offset:0
	v_mfma_f32_32x32x16_bf16 a[80:95], v[176:179], v[192:195], a[80:95]
	s_mov_b32 m0, s24
	s_nop 0
	buffer_load_dwordx4 v196, s[4:7], s30 offen lds
	ds_read_b128 a[208:211], v217 offset:128
	v_mfma_f32_32x32x16_bf16 a[96:111], v[184:187], v[164:167], a[96:111]
	s_mov_b32 m0, s25
	s_nop 0
	buffer_load_dwordx4 v196, s[4:7], s31 offen lds
	ds_read_b128 a[212:215], v199 offset:128
	v_mfma_f32_32x32x16_bf16 a[112:127], v[184:187], v[192:195], a[112:127]
	s_mov_b32 m0, s26
	s_nop 0
	buffer_load_dwordx4 v196, s[4:7], s33 offen lds
	ds_read_b128 a[216:219], v198 offset:128
	v_mfma_f32_32x32x16_bf16 a[0:15], v[172:175], v[128:131], a[0:15]
	ds_read_b128 a[220:223], v197 offset:128
	v_max3_f32 v156, v112, v113, v80
	v_max3_f32 v157, v114, v115, v81
	v_max3_f32 v156, v156, v82, v83
	v_mfma_f32_32x32x16_bf16 a[16:31], v[172:175], v[144:147], a[16:31]
	ds_read_b128 a[224:227], v217 offset:8192
	v_max3_f32 v156, v156, v116, v117
	v_max3_f32 v157, v157, v118, v119
	v_max3_f32 v156, v156, v84, v85
	v_max3_f32 v157, v157, v86, v87
	v_mfma_f32_32x32x16_bf16 a[32:47], v[168:171], v[128:131], a[32:47]
	ds_read_b128 a[228:231], v199 offset:8192
	v_max3_f32 v156, v156, v120, v121
	v_max3_f32 v157, v157, v122, v123
	v_max3_f32 v156, v156, v88, v89
	v_max3_f32 v157, v157, v90, v91
	v_mfma_f32_32x32x16_bf16 a[48:63], v[168:171], v[144:147], a[48:63]
	ds_read_b128 a[232:235], v198 offset:8192
	v_max3_f32 v156, v156, v124, v125
	v_max3_f32 v157, v157, v126, v127
	v_max3_f32 v156, v156, v92, v93
	v_max3_f32 v157, v157, v94, v95
	v_mfma_f32_32x32x16_bf16 a[64:79], v[160:163], v[128:131], a[64:79]
	ds_read_b128 a[236:239], v197 offset:8192
	v_max3_f32 v158, v96, v97, v64
	v_max3_f32 v159, v98, v99, v65
	v_max3_f32 v158, v158, v66, v67
	v_mfma_f32_32x32x16_bf16 a[80:95], v[160:163], v[144:147], a[80:95]
	ds_read_b128 a[240:243], v217 offset:8320
	v_max3_f32 v158, v158, v100, v101
	v_max3_f32 v159, v159, v102, v103
	v_max3_f32 v158, v158, v68, v69
	v_max3_f32 v159, v159, v70, v71
	v_mfma_f32_32x32x16_bf16 a[96:111], v[136:139], v[128:131], a[96:111]
	ds_read_b128 a[244:247], v199 offset:8320
	v_max3_f32 v128, v158, v104, v105
	v_max3_f32 v129, v159, v106, v107
	v_max3_f32 v128, v128, v72, v73
	v_max3_f32 v129, v129, v74, v75
	v_mfma_f32_32x32x16_bf16 a[112:127], v[136:139], v[144:147], a[112:127]
	ds_read_b128 a[248:251], v198 offset:8320
	v_max3_f32 v128, v128, v108, v109
	v_max3_f32 v129, v129, v110, v111
	v_max3_f32 v128, v128, v76, v77
	v_max3_f32 v130, v129, v78, v79
	v_mfma_f32_32x32x16_bf16 a[0:15], v[132:135], v[52:55], a[0:15]
	ds_read_b128 a[252:255], v197 offset:8320
	v_max_f32_e32 v129, v156, v157
	v_mov_b32_e32 v131, v129
	s_nop 1
	v_permlane32_swap_b32_e32 v129, v131
	v_max_f32_e32 v129, v129, v131
	v_mfma_f32_32x32x16_bf16 a[16:31], v[132:135], v[140:143], a[16:31]
	v_max_f32_e32 v128, v128, v130
	v_mov_b32_e32 v130, v128
	s_nop 1
	v_permlane32_swap_b32_e32 v128, v130
	v_max_f32_e32 v128, v128, v130
	v_max_f32_e32 v130, v129, v129
	v_max_f32_e32 v131, v128, v128
	v_max_f32_e32 v130, v130, v131
	s_mov_b32 s0, 0x41000000
	v_mfma_f32_32x32x16_bf16 a[32:47], v[60:63], v[52:55], a[32:47]
	v_cmp_lt_f32_e32 vcc, s0, v130
	s_cmp_lg_u64 vcc, 0
	s_cselect_b64 s[0:1], -1, 0
	s_cbranch_vccnz .LBB0_43

.LBB0_38:
	s_waitcnt lgkmcnt(0)
	v_mfma_f32_32x32x16_bf16 v[112:127], a[192:195], a[128:131], v[0:15]
	ds_read_b64_tr_b16 v[172:173], v212 offset:0
	v_exp_f32_e32 v227, v80
	v_exp_f32_e32 v228, v81
	v_cvt_pk_bf16_f32 v164, v128, v129
	v_exp_f32_e32 v82, v82
	v_exp_f32_e32 v83, v83
	v_mfma_f32_32x32x16_bf16 v[96:111], a[192:195], a[160:163], v[16:31]
	ds_read_b64_tr_b16 v[174:175], v212 offset:0x800
	v_cvt_pk_bf16_f32 v165, v130, v131
	v_mfma_f32_32x32x16_bf16 v[48:63], a[224:227], a[128:131], v[0:15]
	v_exp_f32_e32 v84, v84
	v_exp_f32_e32 v85, v85
	ds_read_b64_tr_b16 v[180:181], v212 offset:0x200
	v_cvt_pk_bf16_f32 v166, v132, v133
	v_mfma_f32_32x32x16_bf16 v[32:47], a[224:227], a[160:163], v[16:31]
	ds_read_b64_tr_b16 v[182:183], v212 offset:0xa00
	v_exp_f32_e32 v86, v86
	v_exp_f32_e32 v87, v87
	ds_read_b64_tr_b16 v[184:185], v212 offset:0x400
	v_cvt_pk_bf16_f32 v167, v134, v135
	v_exp_f32_e32 v80, v88
	v_exp_f32_e32 v81, v89
	v_mfma_f32_32x32x16_bf16 v[112:127], a[196:199], a[132:135], v[112:127]
	ds_read_b64_tr_b16 v[186:187], v212 offset:0xc00
	v_cvt_pk_bf16_f32 v160, v136, v137
	v_exp_f32_e32 v90, v90
	v_exp_f32_e32 v91, v91
	v_mfma_f32_32x32x16_bf16 v[96:111], a[196:199], a[164:167], v[96:111]
	ds_read_b64_tr_b16 v[192:193], v212 offset:0x600
	v_cvt_pk_bf16_f32 v161, v138, v139
	v_exp_f32_e32 v217, v92
	v_exp_f32_e32 v220, v93
	v_mfma_f32_32x32x16_bf16 v[48:63], a[228:231], a[132:135], v[48:63]
	ds_read_b64_tr_b16 v[194:195], v212 offset:0xe00
	v_cvt_pk_bf16_f32 v162, v140, v141
	v_mfma_f32_32x32x16_bf16 v[32:47], a[228:231], a[164:167], v[32:47]
	ds_read_b64_tr_b16 v[188:189], v212 offset:0x1000
	v_exp_f32_e32 v221, v94
	v_exp_f32_e32 v222, v95
	ds_read_b64_tr_b16 v[190:191], v212 offset:0x1800
	v_cvt_pk_bf16_f32 v163, v142, v143
	v_exp_f32_e32 v130, v64
	v_exp_f32_e32 v131, v65
	v_mfma_f32_32x32x16_bf16 v[112:127], a[200:203], a[136:139], v[112:127]
	ds_read_b64_tr_b16 v[176:177], v212 offset:0x1200
	v_cvt_pk_bf16_f32 v196, v144, v145
	v_exp_f32_e32 v138, v66
	v_exp_f32_e32 v139, v67
	v_mfma_f32_32x32x16_bf16 v[96:111], a[200:203], a[168:171], v[96:111]
	ds_read_b64_tr_b16 v[178:179], v212 offset:0x1a00
	v_cvt_pk_bf16_f32 v197, v146, v147
	v_mfma_f32_32x32x16_bf16 v[48:63], a[232:235], a[136:139], v[48:63]
	ds_read_b64_tr_b16 v[168:169], v212 offset:0x1400
	v_exp_f32_e32 v229, v68
	v_exp_f32_e32 v230, v69
	v_cvt_pk_bf16_f32 v198, v148, v149
	v_mfma_f32_32x32x16_bf16 v[32:47], a[232:235], a[168:171], v[32:47]
	ds_read_b64_tr_b16 v[170:171], v212 offset:0x1c00
	ds_read_b64_tr_b16 v[144:145], v212 offset:0x1600
	v_exp_f32_e32 v231, v70
	v_exp_f32_e32 v232, v71
	v_cvt_pk_bf16_f32 v199, v150, v151
	v_exp_f32_e32 v64, v72
	v_exp_f32_e32 v65, v73
	v_mfma_f32_32x32x16_bf16 v[112:127], a[204:207], a[140:143], v[112:127]
	ds_read_b64_tr_b16 v[146:147], v212 offset:0x1e00
	v_cvt_pk_bf16_f32 v148, v152, v153
	v_exp_f32_e32 v70, v74
	v_exp_f32_e32 v71, v75
	v_mfma_f32_32x32x16_bf16 v[96:111], a[204:207], a[172:175], v[96:111]
	ds_read_b64_tr_b16 v[140:141], v212 offset:0x2000
	v_cvt_pk_bf16_f32 v149, v154, v155
	v_exp_f32_e32 v154, v76
	v_exp_f32_e32 v155, v77
	v_mfma_f32_32x32x16_bf16 v[48:63], a[236:239], a[140:143], v[48:63]
	ds_read_b64_tr_b16 v[142:143], v212 offset:0x2800
	v_cvt_pk_bf16_f32 v150, v156, v157
	v_mfma_f32_32x32x16_bf16 v[32:47], a[236:239], a[172:175], v[32:47]
	ds_read_b64_tr_b16 v[66:67], v212 offset:0x2200
	v_exp_f32_e32 v156, v78
	v_exp_f32_e32 v157, v79
	ds_read_b64_tr_b16 v[68:69], v212 offset:0x2a00
	v_cvt_pk_bf16_f32 v151, v158, v159
	v_mfma_f32_32x32x16_bf16 v[112:127], a[208:211], a[144:147], v[112:127]
	ds_read_b64_tr_b16 v[132:133], v212 offset:0x2400
	v_cvt_pk_bf16_f32 v72, v227, v228
	v_add_f32_e32 v74, v226, v227
	v_add_f32_e32 v75, v224, v228
	s_add_i32 s0, s28, 0x84000
	v_mfma_f32_32x32x16_bf16 v[96:111], a[208:211], a[176:179], v[96:111]
	ds_read_b64_tr_b16 v[134:135], v212 offset:0x2c00
	v_cvt_pk_bf16_f32 v73, v82, v83
	v_add_f32_e32 v78, v74, v82
	v_add_f32_e32 v75, v75, v83
	v_mfma_f32_32x32x16_bf16 v[48:63], a[240:243], a[144:147], v[48:63]
	ds_read_b64_tr_b16 v[76:77], v212 offset:0x2600
	v_cvt_pk_bf16_f32 v74, v84, v85
	v_add_f32_e32 v84, v78, v84
	v_add_f32_e32 v85, v75, v85
	s_add_i32 s1, s28, 0x84400
	v_mfma_f32_32x32x16_bf16 v[32:47], a[240:243], a[176:179], v[32:47]
	ds_read_b64_tr_b16 v[78:79], v212 offset:0x2e00
	ds_read_b64_tr_b16 v[82:83], v212 offset:0x3000
	v_cvt_pk_bf16_f32 v75, v86, v87
	v_add_f32_e32 v86, v84, v86
	v_add_f32_e32 v87, v85, v87
	v_mfma_f32_32x32x16_bf16 v[112:127], a[212:215], a[148:151], v[112:127]
	ds_read_b64_tr_b16 v[84:85], v212 offset:0x3800
	v_add_f32_e32 v88, v86, v80
	v_add_f32_e32 v89, v87, v81
	s_add_i32 s4, s28, 0x84800
	v_mfma_f32_32x32x16_bf16 v[96:111], a[212:215], a[180:183], v[96:111]
	ds_read_b64_tr_b16 v[86:87], v212 offset:0x3200
	v_add_f32_e32 v92, v88, v90
	v_add_f32_e32 v93, v89, v91
	v_mfma_f32_32x32x16_bf16 v[48:63], a[244:247], a[148:151], v[48:63]
	ds_read_b64_tr_b16 v[88:89], v212 offset:0x3a00
	v_add_f32_e32 v128, v92, v217
	v_add_f32_e32 v129, v93, v220
	s_add_i32 s5, s28, 0x84c00
	v_mfma_f32_32x32x16_bf16 v[32:47], a[244:247], a[180:183], v[32:47]
	ds_read_b64_tr_b16 v[92:93], v212 offset:0x3400
	ds_read_b64_tr_b16 v[94:95], v212 offset:0x3c00
	v_add_f32_e32 v152, v128, v221
	v_add_f32_e32 v153, v129, v222
	v_mfma_f32_32x32x16_bf16 v[112:127], a[216:219], a[152:155], v[112:127]
	ds_read_b64_tr_b16 v[128:129], v212 offset:0x3600
	v_cvt_pk_bf16_f32 v136, v130, v131
	v_add_f32_e32 v158, v223, v130
	v_add_f32_e32 v159, v225, v131
	v_mfma_f32_32x32x16_bf16 v[96:111], a[216:219], a[184:187], v[96:111]
	ds_read_b64_tr_b16 v[130:131], v212 offset:0x3e00
	v_cvt_pk_bf16_f32 v137, v138, v139
	v_add_f32_e32 v158, v158, v138
	v_add_f32_e32 v139, v159, v139
	v_mfma_f32_32x32x16_bf16 v[48:63], a[248:251], a[152:155], v[48:63]
	v_cvt_pk_bf16_f32 v138, v229, v230
	v_add_f32_e32 v158, v158, v229
	v_add_f32_e32 v159, v139, v230
	v_mfma_f32_32x32x16_bf16 v[32:47], a[248:251], a[184:187], v[32:47]
	s_add_i32 s6, s28, 0x80080
	v_cvt_pk_bf16_f32 v139, v231, v232
	v_add_f32_e32 v158, v158, v231
	v_add_f32_e32 v159, v159, v232
	v_mfma_f32_32x32x16_bf16 v[112:127], a[220:223], a[156:159], v[112:127]
	v_add_f32_e32 v158, v158, v64
	v_add_f32_e32 v159, v159, v65
	v_mfma_f32_32x32x16_bf16 v[96:111], a[220:223], a[188:191], v[96:111]
	v_add_f32_e32 v158, v158, v70
	v_add_f32_e32 v159, v159, v71
	v_mfma_f32_32x32x16_bf16 v[48:63], a[252:255], a[156:159], v[48:63]
	v_add_f32_e32 v158, v158, v154
	v_add_f32_e32 v159, v159, v155
	v_mfma_f32_32x32x16_bf16 v[32:47], a[252:255], a[188:191], v[32:47]
	s_add_i32 s7, s28, 0x80880
	v_add_f32_e32 v158, v158, v156
	v_add_f32_e32 v159, v159, v157
	v_add_f32_e32 v152, v152, v153
	s_waitcnt vmcnt(0) lgkmcnt(0)
	s_barrier
	v_mfma_f32_32x32x16_bf16 a[0:15], v[172:175], v[164:167], a[0:15]
	v_mov_b32_e32 v153, v152
	v_mfma_f32_32x32x16_bf16 a[16:31], v[172:175], v[196:199], a[16:31]
	s_nop 1
	v_permlane32_swap_b32_e32 v152, v153
	v_add_f32_e32 v152, v152, v153
	v_mfma_f32_32x32x16_bf16 a[32:47], v[180:183], v[164:167], a[32:47]
	v_add_f32_e32 v153, v219, v152
	v_add_f32_e32 v152, v158, v159
	v_mov_b32_e32 v158, v152
	v_mfma_f32_32x32x16_bf16 a[48:63], v[180:183], v[196:199], a[48:63]
	s_nop 1
	v_permlane32_swap_b32_e32 v152, v158
	v_add_f32_e32 v152, v152, v158
	v_mfma_f32_32x32x16_bf16 a[64:79], v[184:187], v[164:167], a[64:79]
	v_add_f32_e32 v152, v218, v152
	v_mfma_f32_32x32x16_bf16 a[80:95], v[184:187], v[196:199], a[80:95]
	v_mfma_f32_32x32x16_bf16 a[96:111], v[192:195], v[164:167], a[96:111]
	v_mfma_f32_32x32x16_bf16 a[112:127], v[192:195], v[196:199], a[112:127]
	v_mfma_f32_32x32x16_bf16 a[0:15], v[188:191], v[160:163], a[0:15]
	v_max3_f32 v158, v112, v113, v48
	v_max3_f32 v159, v114, v115, v49
	v_max3_f32 v158, v158, v50, v51
	v_mfma_f32_32x32x16_bf16 a[16:31], v[188:191], v[148:151], a[16:31]
	v_max3_f32 v158, v158, v116, v117
	v_max3_f32 v159, v159, v118, v119
	v_max3_f32 v158, v158, v52, v53
	v_max3_f32 v159, v159, v54, v55
	v_mfma_f32_32x32x16_bf16 a[32:47], v[176:179], v[160:163], a[32:47]
	v_max3_f32 v158, v158, v120, v121
	v_max3_f32 v159, v159, v122, v123
	v_max3_f32 v158, v158, v56, v57
	v_max3_f32 v159, v159, v58, v59
	v_mfma_f32_32x32x16_bf16 a[48:63], v[176:179], v[148:151], a[48:63]
	v_max3_f32 v158, v158, v124, v125
	v_max3_f32 v159, v159, v126, v127
	v_max3_f32 v158, v158, v60, v61
	v_max3_f32 v159, v159, v62, v63
	v_mfma_f32_32x32x16_bf16 a[64:79], v[168:171], v[160:163], a[64:79]
	v_max3_f32 v164, v96, v97, v32
	v_max3_f32 v165, v98, v99, v33
	v_max3_f32 v164, v164, v34, v35
	v_mfma_f32_32x32x16_bf16 a[80:95], v[168:171], v[148:151], a[80:95]
	v_max3_f32 v164, v164, v100, v101
	v_max3_f32 v165, v165, v102, v103
	v_max3_f32 v164, v164, v36, v37
	v_max3_f32 v165, v165, v38, v39
	v_mfma_f32_32x32x16_bf16 a[96:111], v[144:147], v[160:163], a[96:111]
	v_max3_f32 v160, v164, v104, v105
	v_max3_f32 v161, v165, v106, v107
	v_max3_f32 v160, v160, v40, v41
	v_max3_f32 v161, v161, v42, v43
	v_mfma_f32_32x32x16_bf16 a[112:127], v[144:147], v[148:151], a[112:127]
	v_max3_f32 v145, v161, v110, v111
	v_max3_f32 v144, v160, v108, v109
	v_max3_f32 v146, v144, v44, v45
	v_max3_f32 v145, v145, v46, v47
	v_mfma_f32_32x32x16_bf16 a[0:15], v[140:143], v[72:75], a[0:15]
	v_max_f32_e32 v144, v158, v159
	v_mov_b32_e32 v147, v144
	s_nop 1
	v_permlane32_swap_b32_e32 v144, v147
	v_max_f32_e32 v144, v144, v147
	v_mfma_f32_32x32x16_bf16 a[16:31], v[140:143], v[136:139], a[16:31]
	v_max_f32_e32 v140, v146, v145
	v_mov_b32_e32 v141, v140
	s_nop 1
	v_permlane32_swap_b32_e32 v140, v141
	v_max_f32_e32 v140, v140, v141
	v_max_f32_e32 v141, v144, v144
	v_max_f32_e32 v142, v140, v140
	v_max_f32_e32 v141, v141, v142
	s_mov_b32 s0, 0x41000000
	v_mfma_f32_32x32x16_bf16 a[32:47], v[66:69], v[72:75], a[32:47]
	v_cmp_lt_f32_e32 vcc, s0, v141
	s_cmp_lg_u64 vcc, 0
	s_cselect_b64 s[0:1], -1, 0
	s_cbranch_vccnz .LBB0_45
